# nt cache hint on the f32 weight (B operand) loads of the MoE gate/up and down GEMM K-loops
# speedup vs baseline: 1.0177x; 1.0177x over previous
.LBB0_1432:
	s_lshr_b32 s33, s2, 6
	s_lshl_b32 s3, s33, 1
	v_or_b32_e32 v2, s3, v193
	s_and_b32 s36, s33, 4
	s_and_b32 s37, s2, 0xc0
	v_and_or_b32 v3, v2, 3, s36
	s_lshr_b32 s36, s2, 1
	s_or_b32 s2, s37, 32
	v_bitop3_b32 v183, s2, v203, v198 bitop3:0xde
	s_or_b32 s2, s37, 0x100
	v_bitop3_b32 v181, s2, v203, v198 bitop3:0xde
	s_or_b32 s2, s37, 0x120
	s_lshl_b32 s38, s33, 10
	v_bitop3_b32 v172, s2, v203, v198 bitop3:0xde
	s_add_i32 s38, s38, 0
	s_mov_b32 s2, m0
	s_mov_b32 m0, s38
	s_nop 0
	global_load_lds_dwordx4 v34, s[18:19]
	s_mov_b32 m0, s2
	s_add_i32 s2, s38, 0x2000
	s_mov_b32 s39, m0
	s_mov_b32 m0, s2
	s_nop 0
	global_load_lds_dwordx4 v35, s[18:19]
	s_mov_b32 m0, s39
	s_add_i32 s2, s38, 0x4000
	s_mov_b32 s39, m0
	s_mov_b32 m0, s2
	s_nop 0
	global_load_lds_dwordx4 v36, s[18:19]
	s_mov_b32 m0, s39
	s_add_i32 s2, s38, 0x6000
	v_lshlrev_b32_e32 v2, 9, v2
	v_lshlrev_b32_e32 v3, 5, v3
	s_and_b32 s36, s36, 0x7fffff80
	s_mov_b32 s39, m0
	s_mov_b32 m0, s2
	s_nop 0
	global_load_lds_dwordx4 v37, s[18:19]
	s_mov_b32 m0, s39
	s_mul_i32 s2, s33, 0x5800
	v_bitop3_b32 v214, v3, v2, v194 bitop3:0xde
	v_or_b32_e32 v2, s36, v1
	s_mul_hi_u32 s39, s3, 0x2c00
	s_add_u32 s40, s59, s2
	s_waitcnt vmcnt(1)
	v_lshlrev_b32_e32 v38, 7, v2
	s_addc_u32 s41, s73, s39
	global_load_dwordx4 v[2:5], v199, s[40:41] nt
	s_add_i32 s40, s3, 16
	s_add_i32 s83, s2, 0x2c000
	s_mul_hi_u32 s84, s40, 0x2c00
	s_add_u32 s40, s59, s83
	s_addc_u32 s41, s73, s84
	global_load_dwordx4 v[6:9], v199, s[40:41] nt
	s_add_i32 s40, s3, 32
	s_add_i32 s85, s2, 0x58000
	s_mul_hi_u32 s86, s40, 0x2c00
	s_add_u32 s40, s59, s85
	s_addc_u32 s41, s73, s86
	global_load_dwordx4 v[10:13], v199, s[40:41] nt
	s_add_i32 s40, s3, 48
	s_add_i32 s87, s2, 0x84000
	s_mul_hi_u32 s88, s40, 0x2c00
	s_add_u32 s40, s59, s87
	s_addc_u32 s41, s73, s88
	global_load_dwordx4 v[14:17], v199, s[40:41] nt
	s_add_u32 s40, s74, s2
	s_addc_u32 s41, s75, s39
	global_load_dwordx4 v[18:21], v199, s[40:41] nt
	s_add_u32 s40, s74, s83
	s_addc_u32 s41, s75, s84
	global_load_dwordx4 v[22:25], v199, s[40:41] nt
	s_add_u32 s40, s74, s85
	s_addc_u32 s41, s75, s86
	global_load_dwordx4 v[26:29], v199, s[40:41] nt
	s_add_u32 s40, s74, s87
	s_addc_u32 s41, s75, s88
	global_load_dwordx4 v[30:33], v199, s[40:41] nt
	s_add_i32 s40, s38, 0x8000
	v_add_u32_e32 v39, 0x80, v34
	s_mov_b32 s41, m0
	s_mov_b32 m0, s40
	s_nop 0
	global_load_lds_dwordx4 v39, s[18:19]
	s_mov_b32 m0, s41
	v_add_u32_e32 v39, 0x80, v35
	s_add_i32 s40, s38, 0xa000
	s_mov_b32 s41, m0
	s_mov_b32 m0, s40
	s_nop 0
	global_load_lds_dwordx4 v39, s[18:19]
	s_mov_b32 m0, s41
	v_add_u32_e32 v39, 0x80, v36
	s_add_i32 s40, s38, 0xc000
	s_mov_b32 s41, m0
	s_mov_b32 m0, s40
	s_nop 0
	global_load_lds_dwordx4 v39, s[18:19]
	s_mov_b32 m0, s41
	v_add_u32_e32 v39, 0x80, v37
	s_add_i32 s40, s38, 0xe000
	s_mov_b32 s41, m0
	s_mov_b32 m0, s40
	s_nop 0
	global_load_lds_dwordx4 v39, s[18:19]
	s_mov_b32 m0, s41
	s_waitcnt vmcnt(4)
	v_add_u32_e32 v217, s52, v214
	v_cvt_pk_bf16_f32 v2, v2, v3
	v_cvt_pk_bf16_f32 v3, v4, v5
	v_cvt_pk_bf16_f32 v4, v6, v7
	v_cvt_pk_bf16_f32 v5, v8, v9
	v_or_b32_e32 v213, 0x100, v214
	ds_write2st64_b64 v217, v[2:3], v[4:5] offset1:16
	v_cvt_pk_bf16_f32 v2, v10, v11
	v_cvt_pk_bf16_f32 v3, v12, v13
	v_cvt_pk_bf16_f32 v4, v14, v15
	v_cvt_pk_bf16_f32 v5, v16, v17
	ds_write2st64_b64 v217, v[2:3], v[4:5] offset0:32 offset1:48
	v_cvt_pk_bf16_f32 v2, v18, v19
	v_cvt_pk_bf16_f32 v3, v20, v21
	v_add_u32_e32 v6, s52, v213
	v_cvt_pk_bf16_f32 v4, v22, v23
	v_cvt_pk_bf16_f32 v5, v24, v25
	s_add_i32 s40, s3, 64
	s_add_i32 s83, s2, 0xb0000
	ds_write2st64_b64 v6, v[2:3], v[4:5] offset1:16
	v_cvt_pk_bf16_f32 v2, v26, v27
	v_cvt_pk_bf16_f32 v3, v28, v29
	v_cvt_pk_bf16_f32 v4, v30, v31
	v_cvt_pk_bf16_f32 v5, v32, v33
	s_mul_hi_u32 s84, s40, 0x2c00
	s_add_u32 s40, s59, s83
	ds_write2st64_b64 v6, v[2:3], v[4:5] offset0:32 offset1:48
	s_addc_u32 s41, s73, s84
	global_load_dwordx4 v[30:33], v199, s[40:41] nt
	s_add_i32 s40, s3, 0x50
	s_add_i32 s85, s2, 0xdc000
	s_mul_hi_u32 s86, s40, 0x2c00
	s_add_u32 s40, s59, s85
	s_addc_u32 s41, s73, s86
	global_load_dwordx4 v[26:29], v199, s[40:41] nt
	s_add_i32 s40, s3, 0x60
	s_add_i32 s87, s2, 0x108000
	s_mul_hi_u32 s88, s40, 0x2c00
	s_add_u32 s40, s59, s87
	s_addc_u32 s41, s73, s88
	s_addk_i32 s3, 0x70
	s_add_i32 s89, s2, 0x134000
	global_load_dwordx4 v[22:25], v199, s[40:41] nt
	s_mul_hi_u32 s3, s3, 0x2c00
	s_add_u32 s40, s59, s89
	s_addc_u32 s41, s73, s3
	global_load_dwordx4 v[18:21], v199, s[40:41] nt
	s_add_u32 s40, s74, s83
	s_addc_u32 s41, s75, s84
	global_load_dwordx4 v[14:17], v199, s[40:41] nt
	s_add_u32 s40, s74, s85
	s_addc_u32 s41, s75, s86
	global_load_dwordx4 v[10:13], v199, s[40:41] nt
	s_add_u32 s40, s74, s87
	s_addc_u32 s41, s75, s88
	global_load_dwordx4 v[6:9], v199, s[40:41] nt
	s_add_u32 s40, s74, s89
	s_addc_u32 s41, s75, s3
	global_load_dwordx4 v[2:5], v199, s[40:41] nt
	s_mul_hi_u32 s3, s33, 0x5800
	s_add_u32 s40, s74, s2
	s_waitcnt lgkmcnt(0)
	s_barrier
	s_addc_u32 s41, s75, s3
	s_add_u32 s83, s59, s2
	v_add_u32_e32 v221, 0x100, v34
	v_mov_b32_e32 v34, 0
	v_bitop3_b32 v212, s37, v203, v198 bitop3:0xde
	v_or_b32_e32 v215, v38, v196
	s_mov_b32 s39, 0x8000
	v_or_b32_e32 v216, v38, v197
	s_addc_u32 s84, s73, s3
	v_add_u32_e32 v218, 0x100, v37
	v_add_u32_e32 v219, 0x100, v36
	v_add_u32_e32 v220, 0x100, v35
	s_mov_b32 s85, 0x10000
	s_mov_b32 s86, 0
	s_mov_b64 s[2:3], 0
	v_mov_b32_e32 v35, v34
	v_mov_b32_e32 v36, v34
	v_mov_b32_e32 v37, v34
	v_mov_b32_e32 v38, v34
	v_mov_b32_e32 v39, v34
	v_mov_b32_e32 v40, v34
	v_mov_b32_e32 v41, v34
	v_mov_b32_e32 v46, v34
	v_mov_b32_e32 v47, v34
	v_mov_b32_e32 v48, v34
	v_mov_b32_e32 v49, v34
	v_mov_b32_e32 v50, v34
	v_mov_b32_e32 v51, v34
	v_mov_b32_e32 v52, v34
	v_mov_b32_e32 v53, v34
	s_waitcnt vmcnt(0)
	v_mov_b32_e32 v42, v34
	v_mov_b32_e32 v43, v34
	v_mov_b32_e32 v44, v34
	v_mov_b32_e32 v45, v34
	v_mov_b32_e32 v54, v34
	v_mov_b32_e32 v55, v34
	v_mov_b32_e32 v56, v34
	v_mov_b32_e32 v57, v34
	v_mov_b32_e32 v58, v34
	v_mov_b32_e32 v59, v34
	v_mov_b32_e32 v60, v34
	v_mov_b32_e32 v61, v34
	v_mov_b32_e32 v62, v34
	v_mov_b32_e32 v63, v34
	v_mov_b32_e32 v64, v34
	v_mov_b32_e32 v65, v34
	v_mov_b32_e32 v66, v34
	v_mov_b32_e32 v67, v34
	v_mov_b32_e32 v68, v34
	v_mov_b32_e32 v69, v34
	v_mov_b32_e32 v70, v34
	v_mov_b32_e32 v71, v34
	v_mov_b32_e32 v72, v34
	v_mov_b32_e32 v73, v34
	v_mov_b32_e32 v74, v34
	v_mov_b32_e32 v75, v34
	v_mov_b32_e32 v76, v34
	v_mov_b32_e32 v77, v34
	v_mov_b32_e32 v78, v34
	v_mov_b32_e32 v79, v34
	v_mov_b32_e32 v80, v34
	v_mov_b32_e32 v81, v34
	v_mov_b32_e32 v82, v34
	v_mov_b32_e32 v83, v34
	v_mov_b32_e32 v84, v34
	v_mov_b32_e32 v85, v34
	v_mov_b32_e32 v86, v34
	v_mov_b32_e32 v87, v34
	v_mov_b32_e32 v88, v34
	v_mov_b32_e32 v89, v34
	v_mov_b32_e32 v90, v34
	v_mov_b32_e32 v91, v34
	v_mov_b32_e32 v92, v34
	v_mov_b32_e32 v93, v34
	v_mov_b32_e32 v94, v34
	v_mov_b32_e32 v95, v34
	v_mov_b32_e32 v96, v34
	v_mov_b32_e32 v97, v34
	v_mov_b32_e32 v98, v34
	v_mov_b32_e32 v99, v34
	v_mov_b32_e32 v100, v34
	v_mov_b32_e32 v101, v34
	v_mov_b32_e32 v102, v34
	v_mov_b32_e32 v103, v34
	v_mov_b32_e32 v104, v34
	v_mov_b32_e32 v105, v34
	v_mov_b32_e32 v106, v34
	v_mov_b32_e32 v107, v34
	v_mov_b32_e32 v108, v34
	v_mov_b32_e32 v109, v34
	v_mov_b32_e32 v110, v34
	v_mov_b32_e32 v111, v34
	v_mov_b32_e32 v112, v34
	v_mov_b32_e32 v113, v34
	v_mov_b32_e32 v114, v34
	v_mov_b32_e32 v115, v34
	v_mov_b32_e32 v116, v34
	v_mov_b32_e32 v117, v34
	v_mov_b32_e32 v118, v34
	v_mov_b32_e32 v119, v34
	v_mov_b32_e32 v120, v34
	v_mov_b32_e32 v121, v34
	v_mov_b32_e32 v122, v34
	v_mov_b32_e32 v123, v34
	v_mov_b32_e32 v124, v34
	v_mov_b32_e32 v125, v34
	v_mov_b32_e32 v126, v34
	v_mov_b32_e32 v127, v34
	v_mov_b32_e32 v128, v34
	v_mov_b32_e32 v129, v34
	v_mov_b32_e32 v130, v34
	v_mov_b32_e32 v131, v34
	v_mov_b32_e32 v132, v34
	v_mov_b32_e32 v133, v34
	v_mov_b32_e32 v134, v34
	v_mov_b32_e32 v135, v34
	v_mov_b32_e32 v136, v34
	v_mov_b32_e32 v137, v34
	v_mov_b32_e32 v138, v34
	v_mov_b32_e32 v139, v34
	v_mov_b32_e32 v140, v34
	v_mov_b32_e32 v141, v34
	v_mov_b32_e32 v142, v34
	v_mov_b32_e32 v143, v34
	v_mov_b32_e32 v144, v34
	v_mov_b32_e32 v145, v34
	v_mov_b32_e32 v146, v34
	v_mov_b32_e32 v147, v34
	v_mov_b32_e32 v148, v34
	v_mov_b32_e32 v149, v34
	v_mov_b32_e32 v150, v34
	v_mov_b32_e32 v151, v34
	v_mov_b32_e32 v152, v34
	v_mov_b32_e32 v153, v34
	v_mov_b32_e32 v154, v34
	v_mov_b32_e32 v155, v34
	v_mov_b32_e32 v156, v34
	v_mov_b32_e32 v157, v34
	v_mov_b32_e32 v158, v34
	v_mov_b32_e32 v159, v34
	v_mov_b32_e32 v160, v34
	v_mov_b32_e32 v161, v34
.LBB0_1433:
	s_add_i32 s88, s39, 0xffff8000
	s_and_b32 s88, s88, 0x8000
	s_add_i32 s88, s88, 0
	s_add_i32 s87, s86, 0
	s_add_i32 s88, s88, 0x18000
	v_add_u32_e32 v246, s88, v212
	v_add_u32_e32 v247, s87, v215
	v_add_u32_e32 v252, s88, v181
	v_add_u32_e32 v254, s88, v172
	v_add_u32_e32 v250, s88, v183
	ds_read_b64_tr_b16 v[222:223], v246
	ds_read_b64_tr_b16 v[224:225], v246 offset:2048
	ds_read_b64_tr_b16 v[226:227], v250
	ds_read_b64_tr_b16 v[228:229], v250 offset:2048
	ds_read_b128 v[162:165], v247
	ds_read_b128 v[166:169], v247 offset:2048
	ds_read_b64_tr_b16 v[230:231], v252
	ds_read_b64_tr_b16 v[232:233], v252 offset:2048
	ds_read_b64_tr_b16 v[234:235], v254
	ds_read_b64_tr_b16 v[236:237], v254 offset:2048
	s_waitcnt lgkmcnt(5)
	v_mfma_f32_16x16x32_bf16 v[62:65], v[222:225], v[162:165], v[62:65]
	ds_read_b128 v[238:241], v247 offset:4096
	s_and_b32 s88, s39, 0x8000
	s_add_i32 s89, s38, s85
	v_mfma_f32_16x16x32_bf16 v[58:61], v[226:229], v[162:165], v[58:61]
	s_mov_b32 s90, m0
	s_mov_b32 m0, s89
	s_nop 0
	global_load_lds_dwordx4 v221, s[18:19]
	s_mov_b32 m0, s90
	s_waitcnt lgkmcnt(3)
	v_mfma_f32_16x16x32_bf16 v[54:57], v[230:233], v[162:165], v[54:57]
	s_waitcnt lgkmcnt(1)
	v_mfma_f32_16x16x32_bf16 v[42:45], v[234:237], v[162:165], v[42:45]
	v_mfma_f32_16x16x32_bf16 v[50:53], v[222:225], v[166:169], v[50:53]
	ds_read_b128 v[162:165], v247 offset:6144
	s_add_i32 s90, s89, 0x2000
	s_mov_b32 s91, m0
	s_mov_b32 m0, s90
	s_nop 0
	global_load_lds_dwordx4 v220, s[18:19]
	s_mov_b32 m0, s91
	v_mfma_f32_16x16x32_bf16 v[46:49], v[226:229], v[166:169], v[46:49]
	v_mfma_f32_16x16x32_bf16 v[38:41], v[230:233], v[166:169], v[38:41]
	v_mfma_f32_16x16x32_bf16 v[34:37], v[234:237], v[166:169], v[34:37]
	s_waitcnt lgkmcnt(1)
	v_mfma_f32_16x16x32_bf16 v[66:69], v[222:225], v[238:241], v[66:69]
	ds_read_b128 v[166:169], v247 offset:8192
	s_add_i32 s90, s89, 0x4000
	s_mov_b32 s91, m0
	s_mov_b32 m0, s90
	s_nop 0
	global_load_lds_dwordx4 v219, s[18:19]
	s_mov_b32 m0, s91
	v_mfma_f32_16x16x32_bf16 v[70:73], v[226:229], v[238:241], v[70:73]
	v_mfma_f32_16x16x32_bf16 v[74:77], v[230:233], v[238:241], v[74:77]
	v_mfma_f32_16x16x32_bf16 v[78:81], v[234:237], v[238:241], v[78:81]
	s_waitcnt lgkmcnt(1)
	v_mfma_f32_16x16x32_bf16 v[82:85], v[222:225], v[162:165], v[82:85]
	ds_read_b128 v[238:241], v247 offset:10240
	s_addk_i32 s89, 0x6000
	s_mov_b32 s90, m0
	s_mov_b32 m0, s89
	s_nop 0
	global_load_lds_dwordx4 v218, s[18:19]
	s_mov_b32 m0, s90
	v_mfma_f32_16x16x32_bf16 v[86:89], v[226:229], v[162:165], v[86:89]
	v_mfma_f32_16x16x32_bf16 v[90:93], v[230:233], v[162:165], v[90:93]
	v_mfma_f32_16x16x32_bf16 v[94:97], v[234:237], v[162:165], v[94:97]
	ds_read_b128 v[242:245], v247 offset:12288
	ds_read_b64_tr_b16 v[162:163], v246 offset:16384
	ds_read_b64_tr_b16 v[164:165], v246 offset:18432
	s_waitcnt lgkmcnt(4)
	v_mfma_f32_16x16x32_bf16 v[98:101], v[222:225], v[166:169], v[98:101]
	v_mfma_f32_16x16x32_bf16 v[102:105], v[226:229], v[166:169], v[102:105]
	v_mfma_f32_16x16x32_bf16 v[106:109], v[230:233], v[166:169], v[106:109]
	v_mfma_f32_16x16x32_bf16 v[110:113], v[234:237], v[166:169], v[110:113]
	ds_read_b128 v[246:249], v247 offset:14336
	ds_read_b64_tr_b16 v[166:167], v250 offset:16384
	ds_read_b64_tr_b16 v[168:169], v250 offset:18432
	s_waitcnt lgkmcnt(6)
	v_mfma_f32_16x16x32_bf16 v[114:117], v[222:225], v[238:241], v[114:117]
	v_mfma_f32_16x16x32_bf16 v[118:121], v[226:229], v[238:241], v[118:121]
	v_mfma_f32_16x16x32_bf16 v[122:125], v[230:233], v[238:241], v[122:125]
	v_mfma_f32_16x16x32_bf16 v[126:129], v[234:237], v[238:241], v[126:129]
	v_add_u32_e32 v200, s87, v216
	ds_read_b128 v[238:241], v200
	ds_read_b64_tr_b16 v[250:251], v252 offset:16384
	ds_read_b64_tr_b16 v[252:253], v252 offset:18432
	s_waitcnt lgkmcnt(8)
	v_mfma_f32_16x16x32_bf16 v[130:133], v[222:225], v[242:245], v[130:133]
	v_mfma_f32_16x16x32_bf16 v[134:137], v[226:229], v[242:245], v[134:137]
	v_mfma_f32_16x16x32_bf16 v[138:141], v[230:233], v[242:245], v[138:141]
	v_mfma_f32_16x16x32_bf16 v[142:145], v[234:237], v[242:245], v[142:145]
	s_waitcnt lgkmcnt(5)
	v_mfma_f32_16x16x32_bf16 v[146:149], v[222:225], v[246:249], v[146:149]
	v_mfma_f32_16x16x32_bf16 v[150:153], v[226:229], v[246:249], v[150:153]
	ds_read_b128 v[222:225], v200 offset:2048
	ds_read_b64_tr_b16 v[226:227], v254 offset:16384
	ds_read_b64_tr_b16 v[228:229], v254 offset:18432
	v_mfma_f32_16x16x32_bf16 v[154:157], v[230:233], v[246:249], v[154:157]
	v_mfma_f32_16x16x32_bf16 v[158:161], v[234:237], v[246:249], v[158:161]
	ds_read_b128 v[230:233], v200 offset:4096
	s_waitcnt lgkmcnt(6)
	v_mfma_f32_16x16x32_bf16 v[62:65], v[162:165], v[238:241], v[62:65]
	s_add_u32 s87, s83, s2
	s_waitcnt vmcnt(11)
	s_addc_u32 s90, s84, s3
	v_mfma_f32_16x16x32_bf16 v[58:61], v[166:169], v[238:241], v[58:61]
	v_cvt_pk_bf16_f32 v30, v30, v31
	v_cvt_pk_bf16_f32 v31, v32, v33
	v_add_u32_e32 v242, s88, v217
	s_waitcnt lgkmcnt(4)
	v_mfma_f32_16x16x32_bf16 v[54:57], v[250:253], v[238:241], v[54:57]
	s_add_u32 s88, s87, 0x160000
	ds_write_b64 v242, v[30:31]
	s_addc_u32 s89, s90, 0
	s_waitcnt lgkmcnt(2)
	v_mfma_f32_16x16x32_bf16 v[42:45], v[226:229], v[238:241], v[42:45]
	global_load_dwordx4 v[30:33], v199, s[88:89] nt
	v_mfma_f32_16x16x32_bf16 v[50:53], v[162:165], v[222:225], v[50:53]
	ds_read_b128 v[234:237], v200 offset:6144
	s_waitcnt vmcnt(11)
	s_add_u32 s88, s87, 0x18c000
	v_mfma_f32_16x16x32_bf16 v[46:49], v[166:169], v[222:225], v[46:49]
	v_cvt_pk_bf16_f32 v26, v26, v27
	v_cvt_pk_bf16_f32 v27, v28, v29
	ds_write_b64 v242, v[26:27] offset:8192
	v_mfma_f32_16x16x32_bf16 v[38:41], v[250:253], v[222:225], v[38:41]
	s_addc_u32 s89, s90, 0
	global_load_dwordx4 v[26:29], v199, s[88:89] nt
	v_mfma_f32_16x16x32_bf16 v[34:37], v[226:229], v[222:225], v[34:37]
	s_waitcnt lgkmcnt(3)
	v_mfma_f32_16x16x32_bf16 v[66:69], v[162:165], v[230:233], v[66:69]
	ds_read_b128 v[222:225], v200 offset:8192
	s_waitcnt vmcnt(11)
	s_add_u32 s88, s87, 0x1b8000
	v_mfma_f32_16x16x32_bf16 v[70:73], v[166:169], v[230:233], v[70:73]
	v_cvt_pk_bf16_f32 v22, v22, v23
	v_cvt_pk_bf16_f32 v23, v24, v25
	ds_write_b64 v242, v[22:23] offset:16384
	v_mfma_f32_16x16x32_bf16 v[74:77], v[250:253], v[230:233], v[74:77]
	s_addc_u32 s89, s90, 0
	global_load_dwordx4 v[22:25], v199, s[88:89] nt
	v_mfma_f32_16x16x32_bf16 v[78:81], v[226:229], v[230:233], v[78:81]
	s_waitcnt lgkmcnt(3)
	v_mfma_f32_16x16x32_bf16 v[82:85], v[162:165], v[234:237], v[82:85]
	ds_read_b128 v[230:233], v200 offset:10240
	s_waitcnt vmcnt(11)
	s_add_u32 s88, s87, 0x1e4000
	v_mfma_f32_16x16x32_bf16 v[86:89], v[166:169], v[234:237], v[86:89]
	v_cvt_pk_bf16_f32 v18, v18, v19
	v_cvt_pk_bf16_f32 v19, v20, v21
	ds_write_b64 v242, v[18:19] offset:24576
	v_mfma_f32_16x16x32_bf16 v[90:93], v[250:253], v[234:237], v[90:93]
	s_addc_u32 s89, s90, 0
	global_load_dwordx4 v[18:21], v199, s[88:89] nt
	v_mfma_f32_16x16x32_bf16 v[94:97], v[226:229], v[234:237], v[94:97]
	ds_read_b128 v[234:237], v200 offset:12288
	s_waitcnt lgkmcnt(4)
	v_mfma_f32_16x16x32_bf16 v[98:101], v[162:165], v[222:225], v[98:101]
	s_add_u32 s87, s40, s2
	s_waitcnt vmcnt(11)
	s_addc_u32 s90, s41, s3
	v_mfma_f32_16x16x32_bf16 v[102:105], v[166:169], v[222:225], v[102:105]
	v_cvt_pk_bf16_f32 v14, v14, v15
	v_cvt_pk_bf16_f32 v15, v16, v17
	s_add_u32 s88, s87, 0x160000
	v_mfma_f32_16x16x32_bf16 v[106:109], v[250:253], v[222:225], v[106:109]
	ds_write_b64 v242, v[14:15] offset:256
	s_addc_u32 s89, s90, 0
	global_load_dwordx4 v[14:17], v199, s[88:89] nt
	v_mfma_f32_16x16x32_bf16 v[110:113], v[226:229], v[222:225], v[110:113]
	s_waitcnt lgkmcnt(3)
	v_mfma_f32_16x16x32_bf16 v[114:117], v[162:165], v[230:233], v[114:117]
	ds_read_b128 v[222:225], v200 offset:14336
	s_waitcnt vmcnt(11)
	s_add_u32 s88, s87, 0x18c000
	v_mfma_f32_16x16x32_bf16 v[118:121], v[166:169], v[230:233], v[118:121]
	v_cvt_pk_bf16_f32 v10, v10, v11
	v_cvt_pk_bf16_f32 v11, v12, v13
	ds_write_b64 v242, v[10:11] offset:8448
	v_mfma_f32_16x16x32_bf16 v[122:125], v[250:253], v[230:233], v[122:125]
	s_addc_u32 s89, s90, 0
	global_load_dwordx4 v[10:13], v199, s[88:89] nt
	v_mfma_f32_16x16x32_bf16 v[126:129], v[226:229], v[230:233], v[126:129]
	s_waitcnt lgkmcnt(3)
	v_mfma_f32_16x16x32_bf16 v[130:133], v[162:165], v[234:237], v[130:133]
	s_waitcnt vmcnt(11)
	s_add_u32 s88, s87, 0x1b8000
	v_cvt_pk_bf16_f32 v6, v6, v7
	v_mfma_f32_16x16x32_bf16 v[134:137], v[166:169], v[234:237], v[134:137]
	v_cvt_pk_bf16_f32 v7, v8, v9
	ds_write_b64 v242, v[6:7] offset:16640
	s_addc_u32 s89, s90, 0
	v_mfma_f32_16x16x32_bf16 v[138:141], v[250:253], v[234:237], v[138:141]
	global_load_dwordx4 v[6:9], v199, s[88:89] nt
	v_mfma_f32_16x16x32_bf16 v[142:145], v[226:229], v[234:237], v[142:145]
	s_waitcnt lgkmcnt(2)
	v_mfma_f32_16x16x32_bf16 v[146:149], v[162:165], v[222:225], v[146:149]
	s_waitcnt vmcnt(11)
	s_add_u32 s88, s87, 0x1e4000
	v_cvt_pk_bf16_f32 v2, v2, v3
	v_mfma_f32_16x16x32_bf16 v[150:153], v[166:169], v[222:225], v[150:153]
	v_cvt_pk_bf16_f32 v3, v4, v5
	ds_write_b64 v242, v[2:3] offset:24832
	s_addc_u32 s89, s90, 0
	v_mfma_f32_16x16x32_bf16 v[154:157], v[250:253], v[222:225], v[154:157]
	global_load_dwordx4 v[2:5], v199, s[88:89] nt
	v_mfma_f32_16x16x32_bf16 v[158:161], v[226:229], v[222:225], v[158:161]
	s_add_i32 s87, s86, 0x8000
	s_cmp_lg_u32 s86, 0x10000
	s_cselect_b32 s86, s87, 0
	s_add_i32 s87, s85, 0x8000
	s_cmp_lg_u32 s85, 0x10000
	s_waitcnt lgkmcnt(0)
	s_barrier
	s_cselect_b32 s85, s87, 0
	s_add_u32 s2, s2, 0xb0000
	s_addc_u32 s3, s3, 0
	s_add_i32 s39, s39, 0x8000
	v_add_u32_e32 v218, 0x80, v218
	v_add_u32_e32 v219, 0x80, v219
	v_add_u32_e32 v220, 0x80, v220
	s_cmp_lg_u32 s2, 0x14a0000
	v_add_u32_e32 v221, 0x80, v221
	s_cbranch_scc1 .LBB0_1433
	v_add_u32_e32 v200, s52, v212
	v_add_u32_e32 v250, 0, v215
	v_add_u32_e32 v215, s52, v181
	v_add_u32_e32 v251, s52, v172
	v_add_u32_e32 v217, s52, v183
	ds_read_b64_tr_b16 v[162:163], v200
	ds_read_b64_tr_b16 v[164:165], v200 offset:2048
	ds_read_b64_tr_b16 v[166:167], v217
	ds_read_b64_tr_b16 v[168:169], v217 offset:2048
	ds_read_b128 v[218:221], v250
	ds_read_b128 v[222:225], v250 offset:2048
	ds_read_b64_tr_b16 v[226:227], v215
	ds_read_b64_tr_b16 v[228:229], v215 offset:2048
	ds_read_b64_tr_b16 v[230:231], v251
	ds_read_b64_tr_b16 v[232:233], v251 offset:2048
	s_waitcnt lgkmcnt(5)
	v_mfma_f32_16x16x32_bf16 v[62:65], v[162:165], v[218:221], v[62:65]
	ds_read_b128 v[234:237], v250 offset:4096
	v_mfma_f32_16x16x32_bf16 v[58:61], v[166:169], v[218:221], v[58:61]
	s_waitcnt lgkmcnt(3)
	v_mfma_f32_16x16x32_bf16 v[54:57], v[226:229], v[218:221], v[54:57]
	s_waitcnt lgkmcnt(1)
	v_mfma_f32_16x16x32_bf16 v[42:45], v[230:233], v[218:221], v[42:45]
	v_mfma_f32_16x16x32_bf16 v[50:53], v[162:165], v[222:225], v[50:53]
	ds_read_b128 v[218:221], v250 offset:6144
	v_mfma_f32_16x16x32_bf16 v[46:49], v[166:169], v[222:225], v[46:49]
	v_mfma_f32_16x16x32_bf16 v[38:41], v[226:229], v[222:225], v[38:41]
	v_mfma_f32_16x16x32_bf16 v[34:37], v[230:233], v[222:225], v[34:37]
	s_waitcnt lgkmcnt(1)
	v_mfma_f32_16x16x32_bf16 v[66:69], v[162:165], v[234:237], v[66:69]
	ds_read_b128 v[222:225], v250 offset:8192
	v_mfma_f32_16x16x32_bf16 v[70:73], v[166:169], v[234:237], v[70:73]
	v_mfma_f32_16x16x32_bf16 v[74:77], v[226:229], v[234:237], v[74:77]
	v_mfma_f32_16x16x32_bf16 v[78:81], v[230:233], v[234:237], v[78:81]
	s_waitcnt lgkmcnt(1)
	v_mfma_f32_16x16x32_bf16 v[82:85], v[162:165], v[218:221], v[82:85]
	ds_read_b128 v[234:237], v250 offset:10240
	v_mfma_f32_16x16x32_bf16 v[86:89], v[166:169], v[218:221], v[86:89]
	v_mfma_f32_16x16x32_bf16 v[90:93], v[226:229], v[218:221], v[90:93]
	v_mfma_f32_16x16x32_bf16 v[94:97], v[230:233], v[218:221], v[94:97]
	ds_read_b128 v[218:221], v250 offset:12288
	ds_read_b64_tr_b16 v[238:239], v200 offset:16384
	ds_read_b64_tr_b16 v[240:241], v200 offset:18432
	s_waitcnt lgkmcnt(4)
	v_mfma_f32_16x16x32_bf16 v[98:101], v[162:165], v[222:225], v[98:101]
	v_mfma_f32_16x16x32_bf16 v[102:105], v[166:169], v[222:225], v[102:105]
	v_mfma_f32_16x16x32_bf16 v[106:109], v[226:229], v[222:225], v[106:109]
	v_mfma_f32_16x16x32_bf16 v[110:113], v[230:233], v[222:225], v[110:113]
	ds_read_b128 v[222:225], v250 offset:14336
	ds_read_b64_tr_b16 v[242:243], v217 offset:16384
	ds_read_b64_tr_b16 v[244:245], v217 offset:18432
	s_waitcnt lgkmcnt(6)
	v_mfma_f32_16x16x32_bf16 v[114:117], v[162:165], v[234:237], v[114:117]
	v_mfma_f32_16x16x32_bf16 v[118:121], v[166:169], v[234:237], v[118:121]
	v_mfma_f32_16x16x32_bf16 v[122:125], v[226:229], v[234:237], v[122:125]
	v_mfma_f32_16x16x32_bf16 v[126:129], v[230:233], v[234:237], v[126:129]
	v_add_u32_e32 v200, 0, v216
	ds_read_b128 v[234:237], v200
	ds_read_b64_tr_b16 v[246:247], v215 offset:16384
	ds_read_b64_tr_b16 v[248:249], v215 offset:18432
	s_waitcnt lgkmcnt(8)
	v_mfma_f32_16x16x32_bf16 v[130:133], v[162:165], v[218:221], v[130:133]
	v_mfma_f32_16x16x32_bf16 v[134:137], v[166:169], v[218:221], v[134:137]
	v_mfma_f32_16x16x32_bf16 v[138:141], v[226:229], v[218:221], v[138:141]
	v_mfma_f32_16x16x32_bf16 v[142:145], v[230:233], v[218:221], v[142:145]
	s_waitcnt lgkmcnt(5)
	v_mfma_f32_16x16x32_bf16 v[146:149], v[162:165], v[222:225], v[146:149]
	v_mfma_f32_16x16x32_bf16 v[150:153], v[166:169], v[222:225], v[150:153]
	ds_read_b128 v[162:165], v200 offset:2048
	ds_read_b64_tr_b16 v[166:167], v251 offset:16384
	ds_read_b64_tr_b16 v[168:169], v251 offset:18432
	v_mfma_f32_16x16x32_bf16 v[154:157], v[226:229], v[222:225], v[154:157]
	v_mfma_f32_16x16x32_bf16 v[158:161], v[230:233], v[222:225], v[158:161]
	ds_read_b128 v[216:219], v200 offset:4096
	s_waitcnt vmcnt(7)
	v_add_u32_e32 v214, s56, v214
	v_cvt_pk_bf16_f32 v30, v30, v31
	v_cvt_pk_bf16_f32 v31, v32, v33
	s_waitcnt lgkmcnt(6)
	v_mfma_f32_16x16x32_bf16 v[62:65], v[238:241], v[234:237], v[62:65]
	ds_write_b64 v214, v[30:31]
	v_mfma_f32_16x16x32_bf16 v[58:61], v[242:245], v[234:237], v[58:61]
	s_waitcnt lgkmcnt(5)
	v_mfma_f32_16x16x32_bf16 v[54:57], v[246:249], v[234:237], v[54:57]
	s_waitcnt lgkmcnt(2)
	v_mfma_f32_16x16x32_bf16 v[30:33], v[166:169], v[234:237], v[42:45]
	v_mfma_f32_16x16x32_bf16 v[42:45], v[238:241], v[162:165], v[50:53]
	s_nop 2
	ds_read_b128 v[50:53], v200 offset:6144
	s_waitcnt vmcnt(6)
	v_mfma_f32_16x16x32_bf16 v[46:49], v[242:245], v[162:165], v[46:49]
	v_cvt_pk_bf16_f32 v26, v26, v27
	v_cvt_pk_bf16_f32 v27, v28, v29
	ds_write_b64 v214, v[26:27] offset:8192
	v_mfma_f32_16x16x32_bf16 v[38:41], v[246:249], v[162:165], v[38:41]
	v_mfma_f32_16x16x32_bf16 v[26:29], v[166:169], v[162:165], v[34:37]
	s_waitcnt lgkmcnt(3)
	v_mfma_f32_16x16x32_bf16 v[34:37], v[238:241], v[216:219], v[66:69]
	v_mfma_f32_16x16x32_bf16 v[66:69], v[242:245], v[216:219], v[70:73]
	s_nop 2
	ds_read_b128 v[70:73], v200 offset:8192
	s_waitcnt vmcnt(5)
	v_mfma_f32_16x16x32_bf16 v[74:77], v[246:249], v[216:219], v[74:77]
	v_cvt_pk_bf16_f32 v22, v22, v23
	v_cvt_pk_bf16_f32 v23, v24, v25
	ds_write_b64 v214, v[22:23] offset:16384
	v_mfma_f32_16x16x32_bf16 v[22:25], v[166:169], v[216:219], v[78:81]
	s_waitcnt lgkmcnt(3)
	v_mfma_f32_16x16x32_bf16 v[78:81], v[238:241], v[50:53], v[82:85]
	v_mfma_f32_16x16x32_bf16 v[82:85], v[242:245], v[50:53], v[86:89]
	s_nop 2
	ds_read_b128 v[86:89], v200 offset:10240
	s_waitcnt vmcnt(4)
	v_mfma_f32_16x16x32_bf16 v[90:93], v[246:249], v[50:53], v[90:93]
	v_cvt_pk_bf16_f32 v18, v18, v19
	v_cvt_pk_bf16_f32 v19, v20, v21
	ds_write_b64 v214, v[18:19] offset:24576
	v_mfma_f32_16x16x32_bf16 v[18:21], v[166:169], v[50:53], v[94:97]
	s_waitcnt lgkmcnt(3)
	v_mfma_f32_16x16x32_bf16 v[50:53], v[238:241], v[70:73], v[98:101]
	v_add_u32_e32 v162, s56, v213
	s_nop 1
	ds_read_b128 v[98:101], v200 offset:12288
	s_waitcnt vmcnt(3)
	v_mfma_f32_16x16x32_bf16 v[94:97], v[242:245], v[70:73], v[102:105]
	v_cvt_pk_bf16_f32 v14, v14, v15
	v_cvt_pk_bf16_f32 v15, v16, v17
	ds_write_b64 v162, v[14:15]
	v_mfma_f32_16x16x32_bf16 v[102:105], v[246:249], v[70:73], v[106:109]
	v_mfma_f32_16x16x32_bf16 v[14:17], v[166:169], v[70:73], v[110:113]
	s_nop 2
	ds_read_b128 v[110:113], v200 offset:14336
	s_waitcnt vmcnt(2)
	s_waitcnt lgkmcnt(4)
	v_mfma_f32_16x16x32_bf16 v[70:73], v[238:241], v[86:89], v[114:117]
	v_cvt_pk_bf16_f32 v10, v10, v11
	v_cvt_pk_bf16_f32 v11, v12, v13
	ds_write_b64 v162, v[10:11] offset:8192
	v_mfma_f32_16x16x32_bf16 v[106:109], v[242:245], v[86:89], v[118:121]
	v_mfma_f32_16x16x32_bf16 v[114:117], v[246:249], v[86:89], v[122:125]
	v_mfma_f32_16x16x32_bf16 v[10:13], v[166:169], v[86:89], v[126:129]
	s_waitcnt vmcnt(1)
	s_waitcnt lgkmcnt(3)
	v_mfma_f32_16x16x32_bf16 v[86:89], v[238:241], v[98:101], v[130:133]
	v_cvt_pk_bf16_f32 v6, v6, v7
	v_cvt_pk_bf16_f32 v7, v8, v9
	ds_write_b64 v162, v[6:7] offset:16384
	v_mfma_f32_16x16x32_bf16 v[118:121], v[242:245], v[98:101], v[134:137]
	v_mfma_f32_16x16x32_bf16 v[122:125], v[246:249], v[98:101], v[138:141]
	v_mfma_f32_16x16x32_bf16 v[6:9], v[166:169], v[98:101], v[142:145]
	s_waitcnt vmcnt(0)
	s_waitcnt lgkmcnt(2)
	v_mfma_f32_16x16x32_bf16 v[98:101], v[238:241], v[110:113], v[146:149]
	v_cvt_pk_bf16_f32 v2, v2, v3
	v_cvt_pk_bf16_f32 v3, v4, v5
	ds_write_b64 v162, v[2:3] offset:24576
	v_mfma_f32_16x16x32_bf16 v[126:129], v[242:245], v[110:113], v[150:153]
	v_mfma_f32_16x16x32_bf16 v[130:133], v[246:249], v[110:113], v[154:157]
	v_mfma_f32_16x16x32_bf16 v[2:5], v[166:169], v[110:113], v[158:161]
	s_waitcnt lgkmcnt(0)
	s_barrier
	v_add_u32_e32 v168, s56, v212
	v_add_u32_e32 v183, s56, v183
	v_add_u32_e32 v181, s56, v181
	ds_read_b64_tr_b16 v[110:111], v168
	ds_read_b64_tr_b16 v[112:113], v168 offset:2048
	ds_read_b64_tr_b16 v[134:135], v183
	ds_read_b64_tr_b16 v[136:137], v183 offset:2048
	ds_read_b128 v[138:141], v250 offset:32768
	ds_read_b64_tr_b16 v[142:143], v181
	ds_read_b128 v[146:149], v250 offset:34816
	ds_read_b128 v[150:153], v250 offset:36864
	ds_read_b64_tr_b16 v[144:145], v181 offset:2048
	v_add_u32_e32 v172, s56, v172
	ds_read_b64_tr_b16 v[154:155], v172
	ds_read_b64_tr_b16 v[156:157], v172 offset:2048
	s_waitcnt lgkmcnt(6)
	v_mfma_f32_16x16x32_bf16 v[62:65], v[110:113], v[138:141], v[62:65]
	v_mfma_f32_16x16x32_bf16 v[58:61], v[134:137], v[138:141], v[58:61]
	s_waitcnt lgkmcnt(2)
	v_mfma_f32_16x16x32_bf16 v[54:57], v[142:145], v[138:141], v[54:57]
	s_waitcnt lgkmcnt(0)
	v_mfma_f32_16x16x32_bf16 v[30:33], v[154:157], v[138:141], v[30:33]
	v_mfma_f32_16x16x32_bf16 v[42:45], v[110:113], v[146:149], v[42:45]
	ds_read_b128 v[138:141], v250 offset:38912
	v_mfma_f32_16x16x32_bf16 v[46:49], v[134:137], v[146:149], v[46:49]
	v_mfma_f32_16x16x32_bf16 v[38:41], v[142:145], v[146:149], v[38:41]
	v_mfma_f32_16x16x32_bf16 v[26:29], v[154:157], v[146:149], v[26:29]
	v_mfma_f32_16x16x32_bf16 v[34:37], v[110:113], v[150:153], v[34:37]
	ds_read_b128 v[146:149], v250 offset:40960
	v_mfma_f32_16x16x32_bf16 v[66:69], v[134:137], v[150:153], v[66:69]
	v_mfma_f32_16x16x32_bf16 v[74:77], v[142:145], v[150:153], v[74:77]
	v_mfma_f32_16x16x32_bf16 v[22:25], v[154:157], v[150:153], v[22:25]
	s_waitcnt lgkmcnt(1)
	v_mfma_f32_16x16x32_bf16 v[150:153], v[134:137], v[138:141], v[82:85]
	s_nop 2
	ds_read_b128 v[82:85], v250 offset:43008
	v_mfma_f32_16x16x32_bf16 v[78:81], v[110:113], v[138:141], v[78:81]
	v_mfma_f32_16x16x32_bf16 v[18:21], v[154:157], v[138:141], v[18:21]
	v_mfma_f32_16x16x32_bf16 v[158:161], v[142:145], v[138:141], v[90:93]
	s_nop 2
	ds_read_b128 v[90:93], v250 offset:45056
	ds_read_b64_tr_b16 v[166:167], v168 offset:16384
	ds_read_b64_tr_b16 v[168:169], v168 offset:18432
	s_waitcnt lgkmcnt(4)
	v_mfma_f32_16x16x32_bf16 v[50:53], v[110:113], v[146:149], v[50:53]
	v_mfma_f32_16x16x32_bf16 v[14:17], v[154:157], v[146:149], v[14:17]
	v_mfma_f32_16x16x32_bf16 v[138:141], v[134:137], v[146:149], v[94:97]
	v_mfma_f32_16x16x32_bf16 v[162:165], v[142:145], v[146:149], v[102:105]
	s_waitcnt lgkmcnt(3)
	v_mfma_f32_16x16x32_bf16 v[146:149], v[110:113], v[82:85], v[70:73]
	s_nop 2
	ds_read_b128 v[70:73], v250 offset:47104
	ds_read_b64_tr_b16 v[220:221], v183 offset:16384
	ds_read_b64_tr_b16 v[222:223], v183 offset:18432
	v_mfma_f32_16x16x32_bf16 v[10:13], v[154:157], v[82:85], v[10:13]
	v_mfma_f32_16x16x32_bf16 v[212:215], v[134:137], v[82:85], v[106:109]
	v_mfma_f32_16x16x32_bf16 v[216:219], v[142:145], v[82:85], v[114:117]
	ds_read_b128 v[82:85], v200 offset:32768
	ds_read_b64_tr_b16 v[236:237], v181 offset:16384
	ds_read_b64_tr_b16 v[238:239], v181 offset:18432
	s_waitcnt lgkmcnt(8)
	v_mfma_f32_16x16x32_bf16 v[6:9], v[154:157], v[90:93], v[6:9]
	v_mfma_f32_16x16x32_bf16 v[224:227], v[110:113], v[90:93], v[86:89]
	v_mfma_f32_16x16x32_bf16 v[228:231], v[134:137], v[90:93], v[118:121]
	v_mfma_f32_16x16x32_bf16 v[232:235], v[142:145], v[90:93], v[122:125]
	s_waitcnt lgkmcnt(5)
	v_mfma_f32_16x16x32_bf16 v[130:133], v[142:145], v[70:73], v[130:133]
	ds_read_b128 v[86:89], v200 offset:34816
	ds_read_b64_tr_b16 v[142:143], v172 offset:16384
	ds_read_b64_tr_b16 v[144:145], v172 offset:18432
	v_mfma_f32_16x16x32_bf16 v[240:243], v[110:113], v[70:73], v[98:101]
	v_mfma_f32_16x16x32_bf16 v[134:137], v[134:137], v[70:73], v[126:129]
	v_mfma_f32_16x16x32_bf16 v[154:157], v[154:157], v[70:73], v[2:5]
	s_nop 2
	ds_read_b128 v[2:5], v200 offset:36864
	s_waitcnt lgkmcnt(6)
	v_mfma_f32_16x16x32_bf16 v[122:125], v[166:169], v[82:85], v[62:65]
	v_mfma_f32_16x16x32_bf16 v[114:117], v[220:223], v[82:85], v[58:61]
	s_waitcnt lgkmcnt(4)
	v_mfma_f32_16x16x32_bf16 v[126:129], v[236:239], v[82:85], v[54:57]
	s_waitcnt lgkmcnt(1)
	v_mfma_f32_16x16x32_bf16 v[118:121], v[142:145], v[82:85], v[30:33]
	s_nop 2
	ds_read_b128 v[30:33], v200 offset:38912
	v_mfma_f32_16x16x32_bf16 v[106:109], v[166:169], v[86:89], v[42:45]
	v_mfma_f32_16x16x32_bf16 v[98:101], v[220:223], v[86:89], v[46:49]
	v_mfma_f32_16x16x32_bf16 v[110:113], v[236:239], v[86:89], v[38:41]
	v_mfma_f32_16x16x32_bf16 v[102:105], v[142:145], v[86:89], v[26:29]
	s_nop 2
	ds_read_b128 v[26:29], v200 offset:40960
	s_waitcnt lgkmcnt(2)
	v_mfma_f32_16x16x32_bf16 v[90:93], v[166:169], v[2:5], v[34:37]
	v_mfma_f32_16x16x32_bf16 v[82:85], v[220:223], v[2:5], v[66:69]
	v_mfma_f32_16x16x32_bf16 v[94:97], v[236:239], v[2:5], v[74:77]
	v_mfma_f32_16x16x32_bf16 v[86:89], v[142:145], v[2:5], v[22:25]
	ds_read_b128 v[2:5], v200 offset:43008
	s_waitcnt lgkmcnt(2)
	v_mfma_f32_16x16x32_bf16 v[74:77], v[166:169], v[30:33], v[78:81]
	v_mfma_f32_16x16x32_bf16 v[66:69], v[220:223], v[30:33], v[150:153]
	v_mfma_f32_16x16x32_bf16 v[78:81], v[236:239], v[30:33], v[158:161]
	v_mfma_f32_16x16x32_bf16 v[70:73], v[142:145], v[30:33], v[18:21]
	ds_read_b128 v[22:25], v200 offset:45056
	s_waitcnt lgkmcnt(2)
	v_mfma_f32_16x16x32_bf16 v[58:61], v[166:169], v[26:29], v[50:53]
	v_mfma_f32_16x16x32_bf16 v[50:53], v[220:223], v[26:29], v[138:141]
	v_mfma_f32_16x16x32_bf16 v[62:65], v[236:239], v[26:29], v[162:165]
	v_mfma_f32_16x16x32_bf16 v[54:57], v[142:145], v[26:29], v[14:17]
	s_waitcnt lgkmcnt(1)
	v_mfma_f32_16x16x32_bf16 v[42:45], v[166:169], v[2:5], v[146:149]
	ds_read_b128 v[138:141], v200 offset:47104
	v_mfma_f32_16x16x32_bf16 v[34:37], v[220:223], v[2:5], v[212:215]
	v_mfma_f32_16x16x32_bf16 v[46:49], v[236:239], v[2:5], v[216:219]
	v_mfma_f32_16x16x32_bf16 v[38:41], v[142:145], v[2:5], v[10:13]
	s_waitcnt lgkmcnt(1)
	v_mfma_f32_16x16x32_bf16 v[26:29], v[166:169], v[22:25], v[224:227]
	v_mfma_f32_16x16x32_bf16 v[18:21], v[220:223], v[22:25], v[228:231]
	v_mfma_f32_16x16x32_bf16 v[30:33], v[236:239], v[22:25], v[232:235]
	v_mfma_f32_16x16x32_bf16 v[22:25], v[142:145], v[22:25], v[6:9]
	s_waitcnt lgkmcnt(0)
	v_mfma_f32_16x16x32_bf16 v[10:13], v[166:169], v[138:141], v[240:243]
	v_mfma_f32_16x16x32_bf16 v[2:5], v[220:223], v[138:141], v[134:137]
	v_mfma_f32_16x16x32_bf16 v[14:17], v[236:239], v[138:141], v[130:133]
	v_mfma_f32_16x16x32_bf16 v[6:9], v[142:145], v[138:141], v[154:157]
	s_waitcnt lgkmcnt(0)
	s_barrier
	s_nop 0
	v_mov_b32_e32 v130, 0
	s_and_b64 vcc, exec, s[6:7]
	v_mov_b32_e32 v131, 0
	v_mov_b32_e32 v132, 0
	s_cbranch_vccnz .LBB0_1436
	global_load_dword v130, v[184:185], off
	global_load_dword v131, v[186:187], off
	global_load_dword v132, v[188:189], off

.LBB0_1539:
	s_ashr_i32 s10, s16, 5
	s_ashr_i32 s11, s10, 31
	s_mul_i32 s14, s10, 0x580000
	s_mul_hi_i32 s2, s10, 0x580000
	s_add_u32 s14, s19, s14
	s_addc_u32 s15, s20, s2
	s_mul_i32 s17, s10, 0x1600000
	s_mul_hi_i32 s2, s10, 0x1600000
	s_add_u32 s17, s64, s17
	s_addc_u32 s2, s65, s2
	s_lshl_b32 s30, s16, 6
	s_and_b32 s30, s30, 0x700
	s_lshl_b32 s31, s30, 2
	s_add_u32 s17, s17, s31
	s_addc_u32 s38, s2, 0
	s_lshl_b32 s2, s16, 8
	v_readfirstlane_b32 s16, v0
	s_and_b32 s31, s2, 0x300
	s_lshr_b32 s2, s16, 6
	s_lshl_b32 s34, s2, 9
	s_lshl_b32 s33, s2, 5
	s_and_b32 s35, s33, 0x60
	v_mov_b32_e32 v3, s34
	s_lshr_b32 s34, s16, 1
	v_bitop3_b32 v206, s35, v3, v194 bitop3:0xde
	s_and_b32 s35, s34, 0x7fffff80
	s_lshl_b32 s34, s16, 1
	s_and_b32 s34, s34, 0x180
	s_or_b32 s36, s34, 32
	v_or_b32_e32 v2, s31, v171
	v_bitop3_b32 v181, s36, v201, v198 bitop3:0xde
	s_or_b32 s36, s34, 64
	v_mul_u32_u24_e32 v34, 0xb00, v2
	v_bitop3_b32 v179, s36, v201, v198 bitop3:0xde
	s_or_b32 s36, s34, 0x60
	v_or_b32_e32 v2, v34, v177
	v_bitop3_b32 v172, s36, v201, v198 bitop3:0xde
	s_lshl_b32 s36, s2, 10
	v_lshlrev_b32_e32 v35, 1, v2
	s_add_i32 s36, s36, 0
	s_mov_b32 s37, m0
	s_mov_b32 m0, s36
	s_nop 0
	global_load_lds_dwordx4 v35, s[14:15]
	s_mov_b32 m0, s37
	s_add_i32 s37, s36, 0x2000
	v_add_lshl_u32 v36, v190, v34, 1
	s_mov_b32 s39, m0
	s_mov_b32 m0, s37
	s_nop 0
	global_load_lds_dwordx4 v36, s[14:15]
	s_mov_b32 m0, s39
	s_add_i32 s37, s36, 0x4000
	v_add_lshl_u32 v37, v191, v34, 1
	s_mov_b32 s39, m0
	s_mov_b32 m0, s37
	s_nop 0
	global_load_lds_dwordx4 v37, s[14:15]
	s_mov_b32 m0, s39
	s_add_i32 s37, s36, 0x6000
	s_lshl_b64 s[40:41], s[2:3], 13
	s_add_u32 s40, s17, s40
	v_bitop3_b32 v2, s33, v194, v203 bitop3:0x6c
	v_or_b32_e32 v4, s35, v1
	s_addc_u32 s41, s38, s41
	s_waitcnt vmcnt(1)
	v_add_lshl_u32 v38, v192, v34, 1
	v_lshlrev_b32_e32 v39, 7, v4
	v_bitop3_b32 v205, v2, s23, v3 bitop3:0x36
	s_mov_b32 s39, m0
	s_mov_b32 m0, s37
	s_nop 0
	global_load_lds_dwordx4 v38, s[14:15]
	s_mov_b32 m0, s39
	global_load_dwordx4 v[2:5], v199, s[40:41] nt
	s_add_i32 s40, s2, 8
	s_mov_b32 s41, s3
	s_lshl_b64 s[40:41], s[40:41], 13
	s_add_u32 s40, s17, s40
	s_addc_u32 s41, s38, s41
	global_load_dwordx4 v[6:9], v199, s[40:41] nt
	s_add_i32 s40, s2, 16
	s_mov_b32 s41, s3
	s_lshl_b64 s[40:41], s[40:41], 13
	s_add_u32 s40, s17, s40
	s_addc_u32 s41, s38, s41
	global_load_dwordx4 v[10:13], v199, s[40:41] nt
	s_add_i32 s40, s2, 24
	s_mov_b32 s41, s3
	s_lshl_b64 s[40:41], s[40:41], 13
	s_add_u32 s40, s17, s40
	s_addc_u32 s41, s38, s41
	global_load_dwordx4 v[14:17], v199, s[40:41] nt
	s_add_i32 s40, s2, 32
	s_mov_b32 s41, s3
	s_lshl_b64 s[40:41], s[40:41], 13
	s_add_u32 s40, s17, s40
	s_addc_u32 s41, s38, s41
	global_load_dwordx4 v[18:21], v199, s[40:41] nt
	s_add_i32 s40, s2, 40
	s_mov_b32 s41, s3
	s_lshl_b64 s[40:41], s[40:41], 13
	s_add_u32 s40, s17, s40
	s_addc_u32 s41, s38, s41
	global_load_dwordx4 v[22:25], v199, s[40:41] nt
	s_add_i32 s40, s2, 48
	s_mov_b32 s41, s3
	s_lshl_b64 s[40:41], s[40:41], 13
	s_add_u32 s40, s17, s40
	s_addc_u32 s41, s38, s41
	global_load_dwordx4 v[26:29], v199, s[40:41] nt
	s_add_i32 s40, s2, 56
	s_mov_b32 s41, s3
	s_lshl_b64 s[40:41], s[40:41], 13
	s_add_u32 s40, s17, s40
	s_addc_u32 s41, s38, s41
	s_add_i32 s39, s36, 0x8000
	v_or_b32_e32 v35, 0x80, v35
	global_load_dwordx4 v[30:33], v199, s[40:41] nt
	s_mov_b32 s40, m0
	s_mov_b32 m0, s39
	s_nop 0
	global_load_lds_dwordx4 v35, s[14:15]
	s_mov_b32 m0, s40
	v_or_b32_e32 v35, 0x80, v36
	s_add_i32 s39, s36, 0xa000
	s_mov_b32 s40, m0
	s_mov_b32 m0, s39
	s_nop 0
	global_load_lds_dwordx4 v35, s[14:15]
	s_mov_b32 m0, s40
	v_or_b32_e32 v35, 0x80, v37
	s_add_i32 s39, s36, 0xc000
	s_mov_b32 s40, m0
	s_mov_b32 m0, s39
	s_nop 0
	global_load_lds_dwordx4 v35, s[14:15]
	s_mov_b32 m0, s40
	v_or_b32_e32 v35, 0x80, v38
	s_add_i32 s39, s36, 0xe000
	s_mov_b32 s40, m0
	s_mov_b32 m0, s39
	s_nop 0
	global_load_lds_dwordx4 v35, s[14:15]
	s_mov_b32 m0, s40
	s_waitcnt vmcnt(4)
	s_add_i32 s40, s2, 64
	v_cvt_pk_bf16_f32 v2, v2, v3
	v_cvt_pk_bf16_f32 v3, v4, v5
	v_add_u32_e32 v4, s24, v206
	ds_write_b64 v4, v[2:3]
	v_cvt_pk_bf16_f32 v2, v6, v7
	v_cvt_pk_bf16_f32 v3, v8, v9
	v_add_u32_e32 v5, s24, v205
	ds_write_b64 v5, v[2:3] offset:4096
	v_cvt_pk_bf16_f32 v2, v10, v11
	v_cvt_pk_bf16_f32 v3, v12, v13
	ds_write_b64 v4, v[2:3] offset:8192
	v_cvt_pk_bf16_f32 v2, v14, v15
	v_cvt_pk_bf16_f32 v3, v16, v17
	ds_write_b64 v5, v[2:3] offset:12288
	v_cvt_pk_bf16_f32 v2, v18, v19
	v_cvt_pk_bf16_f32 v3, v20, v21
	s_mov_b32 s41, s3
	ds_write_b64 v4, v[2:3] offset:16384
	v_cvt_pk_bf16_f32 v2, v22, v23
	v_cvt_pk_bf16_f32 v3, v24, v25
	s_lshl_b64 s[40:41], s[40:41], 13
	ds_write_b64 v5, v[2:3] offset:20480
	v_cvt_pk_bf16_f32 v2, v26, v27
	v_cvt_pk_bf16_f32 v3, v28, v29
	s_add_u32 s40, s17, s40
	ds_write_b64 v4, v[2:3] offset:24576
	v_cvt_pk_bf16_f32 v2, v30, v31
	v_cvt_pk_bf16_f32 v3, v32, v33
	s_addc_u32 s41, s38, s41
	ds_write_b64 v5, v[2:3] offset:28672
	global_load_dwordx4 v[30:33], v199, s[40:41] nt
	s_add_i32 s40, s2, 0x48
	s_mov_b32 s41, s3
	s_lshl_b64 s[40:41], s[40:41], 13
	s_add_u32 s40, s17, s40
	s_addc_u32 s41, s38, s41
	global_load_dwordx4 v[26:29], v199, s[40:41] nt
	s_add_i32 s40, s2, 0x50
	s_mov_b32 s41, s3
	s_lshl_b64 s[40:41], s[40:41], 13
	s_add_u32 s40, s17, s40
	s_addc_u32 s41, s38, s41
	global_load_dwordx4 v[22:25], v199, s[40:41] nt
	s_add_i32 s40, s2, 0x58
	s_mov_b32 s41, s3
	s_lshl_b64 s[40:41], s[40:41], 13
	s_add_u32 s40, s17, s40
	s_addc_u32 s41, s38, s41
	global_load_dwordx4 v[18:21], v199, s[40:41] nt
	s_add_i32 s40, s2, 0x60
	s_mov_b32 s41, s3
	s_lshl_b64 s[40:41], s[40:41], 13
	s_add_u32 s40, s17, s40
	s_addc_u32 s41, s38, s41
	global_load_dwordx4 v[14:17], v199, s[40:41] nt
	s_add_i32 s40, s2, 0x68
	s_mov_b32 s41, s3
	s_lshl_b64 s[40:41], s[40:41], 13
	s_add_u32 s40, s17, s40
	s_addc_u32 s41, s38, s41
	global_load_dwordx4 v[10:13], v199, s[40:41] nt
	s_add_i32 s40, s2, 0x70
	s_mov_b32 s41, s3
	s_lshl_b64 s[40:41], s[40:41], 13
	s_add_u32 s40, s17, s40
	s_addc_u32 s41, s38, s41
	s_addk_i32 s2, 0x78
	global_load_dwordx4 v[6:9], v199, s[40:41] nt
	s_lshl_b64 s[40:41], s[2:3], 13
	s_add_u32 s40, s17, s40
	s_addc_u32 s41, s38, s41
	global_load_dwordx4 v[2:5], v199, s[40:41] nt
	s_lshl_b64 s[40:41], s[16:17], 7
	s_waitcnt lgkmcnt(0)
	s_barrier
	s_and_b32 s16, s41, 0x7f
	s_and_b32 s2, s40, 0xffffe000
	s_add_u32 s2, s17, s2
	v_lshl_add_u32 v209, v34, 1, v202
	v_mov_b32_e32 v34, 0
	v_bitop3_b32 v183, s34, v201, v198 bitop3:0xde
	v_or_b32_e32 v207, v39, v196
	s_mov_b32 s37, 0x8000
	v_or_b32_e32 v208, v39, v197
	s_addc_u32 s38, s38, s16
	s_mov_b32 s39, 0x10000
	s_mov_b32 s40, 0
	s_mov_b64 s[16:17], 0
	v_mov_b32_e32 v35, v34
	v_mov_b32_e32 v36, v34
	v_mov_b32_e32 v37, v34
	v_mov_b32_e32 v38, v34
	v_mov_b32_e32 v39, v34
	v_mov_b32_e32 v40, v34
	v_mov_b32_e32 v41, v34
	s_waitcnt vmcnt(0)
	v_mov_b32_e32 v42, v34
	v_mov_b32_e32 v43, v34
	v_mov_b32_e32 v44, v34
	v_mov_b32_e32 v45, v34
	v_mov_b32_e32 v46, v34
	v_mov_b32_e32 v47, v34
	v_mov_b32_e32 v48, v34
	v_mov_b32_e32 v49, v34
	v_mov_b32_e32 v50, v34
	v_mov_b32_e32 v51, v34
	v_mov_b32_e32 v52, v34
	v_mov_b32_e32 v53, v34
	v_mov_b32_e32 v54, v34
	v_mov_b32_e32 v55, v34
	v_mov_b32_e32 v56, v34
	v_mov_b32_e32 v57, v34
	v_mov_b32_e32 v58, v34
	v_mov_b32_e32 v59, v34
	v_mov_b32_e32 v60, v34
	v_mov_b32_e32 v61, v34
	v_mov_b32_e32 v62, v34
	v_mov_b32_e32 v63, v34
	v_mov_b32_e32 v64, v34
	v_mov_b32_e32 v65, v34
	v_mov_b32_e32 v66, v34
	v_mov_b32_e32 v67, v34
	v_mov_b32_e32 v68, v34
	v_mov_b32_e32 v69, v34
	v_mov_b32_e32 v70, v34
	v_mov_b32_e32 v71, v34
	v_mov_b32_e32 v72, v34
	v_mov_b32_e32 v73, v34
	v_mov_b32_e32 v74, v34
	v_mov_b32_e32 v75, v34
	v_mov_b32_e32 v76, v34
	v_mov_b32_e32 v77, v34
	v_mov_b32_e32 v78, v34
	v_mov_b32_e32 v79, v34
	v_mov_b32_e32 v80, v34
	v_mov_b32_e32 v81, v34
	v_mov_b32_e32 v82, v34
	v_mov_b32_e32 v83, v34
	v_mov_b32_e32 v84, v34
	v_mov_b32_e32 v85, v34
	v_mov_b32_e32 v86, v34
	v_mov_b32_e32 v87, v34
	v_mov_b32_e32 v88, v34
	v_mov_b32_e32 v89, v34
	v_mov_b32_e32 v90, v34
	v_mov_b32_e32 v91, v34
	v_mov_b32_e32 v92, v34
	v_mov_b32_e32 v93, v34
	v_mov_b32_e32 v94, v34
	v_mov_b32_e32 v95, v34
	v_mov_b32_e32 v96, v34
	v_mov_b32_e32 v97, v34
	v_mov_b32_e32 v98, v34
	v_mov_b32_e32 v99, v34
	v_mov_b32_e32 v100, v34
	v_mov_b32_e32 v101, v34
	v_mov_b32_e32 v102, v34
	v_mov_b32_e32 v103, v34
	v_mov_b32_e32 v104, v34
	v_mov_b32_e32 v105, v34
	v_mov_b32_e32 v106, v34
	v_mov_b32_e32 v107, v34
	v_mov_b32_e32 v108, v34
	v_mov_b32_e32 v109, v34
	v_mov_b32_e32 v110, v34
	v_mov_b32_e32 v111, v34
	v_mov_b32_e32 v112, v34
	v_mov_b32_e32 v113, v34
	v_mov_b32_e32 v114, v34
	v_mov_b32_e32 v115, v34
	v_mov_b32_e32 v116, v34
	v_mov_b32_e32 v117, v34
	v_mov_b32_e32 v118, v34
	v_mov_b32_e32 v119, v34
	v_mov_b32_e32 v120, v34
	v_mov_b32_e32 v121, v34
	v_mov_b32_e32 v122, v34
	v_mov_b32_e32 v123, v34
	v_mov_b32_e32 v124, v34
	v_mov_b32_e32 v125, v34
	v_mov_b32_e32 v126, v34
	v_mov_b32_e32 v127, v34
	v_mov_b32_e32 v128, v34
	v_mov_b32_e32 v129, v34
	v_mov_b32_e32 v130, v34
	v_mov_b32_e32 v131, v34
	v_mov_b32_e32 v132, v34
	v_mov_b32_e32 v133, v34
	v_mov_b32_e32 v134, v34
	v_mov_b32_e32 v135, v34
	v_mov_b32_e32 v136, v34
	v_mov_b32_e32 v137, v34
	v_mov_b32_e32 v138, v34
	v_mov_b32_e32 v139, v34
	v_mov_b32_e32 v140, v34
	v_mov_b32_e32 v141, v34
	v_mov_b32_e32 v142, v34
	v_mov_b32_e32 v143, v34
	v_mov_b32_e32 v144, v34
	v_mov_b32_e32 v145, v34
	v_mov_b32_e32 v146, v34
	v_mov_b32_e32 v147, v34
	v_mov_b32_e32 v148, v34
	v_mov_b32_e32 v149, v34
	v_mov_b32_e32 v150, v34
	v_mov_b32_e32 v151, v34
	v_mov_b32_e32 v152, v34
	v_mov_b32_e32 v153, v34
	v_mov_b32_e32 v158, v34
	v_mov_b32_e32 v159, v34
	v_mov_b32_e32 v160, v34
	v_mov_b32_e32 v161, v34
	v_mov_b32_e32 v154, v34
	v_mov_b32_e32 v155, v34
	v_mov_b32_e32 v156, v34
	v_mov_b32_e32 v157, v34
.LBB0_1540:
	s_add_i32 s42, s37, 0xffff8000
	s_and_b32 s42, s42, 0x8000
	s_add_i32 s41, s40, 0
	s_add_i32 s42, s24, s42
	v_add_u32_e32 v234, s42, v183
	v_add_u32_e32 v235, s41, v207
	v_add_u32_e32 v240, s42, v179
	v_add_u32_e32 v242, s42, v172
	v_add_u32_e32 v238, s42, v181
	ds_read_b64_tr_b16 v[210:211], v234
	ds_read_b64_tr_b16 v[212:213], v234 offset:2048
	ds_read_b64_tr_b16 v[214:215], v238
	ds_read_b64_tr_b16 v[216:217], v238 offset:2048
	ds_read_b128 v[162:165], v235
	ds_read_b128 v[166:169], v235 offset:2048
	ds_read_b64_tr_b16 v[218:219], v240
	ds_read_b64_tr_b16 v[220:221], v240 offset:2048
	ds_read_b64_tr_b16 v[222:223], v242
	ds_read_b64_tr_b16 v[224:225], v242 offset:2048
	s_waitcnt lgkmcnt(5)
	v_mfma_f32_16x16x32_bf16 v[34:37], v[210:213], v[162:165], v[34:37]
	ds_read_b128 v[226:229], v235 offset:4096
	s_and_b32 s42, s37, 0x8000
	v_add_u32_e32 v230, 0xffef8000, v209
	v_mfma_f32_16x16x32_bf16 v[38:41], v[214:217], v[162:165], v[38:41]
	s_add_i32 s43, s36, s39
	s_mov_b32 s44, m0
	s_mov_b32 m0, s43
	s_nop 0
	global_load_lds_dwordx4 v230, s[14:15]
	s_mov_b32 m0, s44
	s_waitcnt lgkmcnt(3)
	v_mfma_f32_16x16x32_bf16 v[42:45], v[218:221], v[162:165], v[42:45]
	s_waitcnt lgkmcnt(1)
	v_mfma_f32_16x16x32_bf16 v[46:49], v[222:225], v[162:165], v[46:49]
	v_mfma_f32_16x16x32_bf16 v[50:53], v[210:213], v[166:169], v[50:53]
	ds_read_b128 v[162:165], v235 offset:6144
	v_add_u32_e32 v230, 0xfff50000, v209
	s_add_i32 s44, s43, 0x2000
	v_mfma_f32_16x16x32_bf16 v[54:57], v[214:217], v[166:169], v[54:57]
	s_mov_b32 s45, m0
	s_mov_b32 m0, s44
	s_nop 0
	global_load_lds_dwordx4 v230, s[14:15]
	s_mov_b32 m0, s45
	v_mfma_f32_16x16x32_bf16 v[58:61], v[218:221], v[166:169], v[58:61]
	v_mfma_f32_16x16x32_bf16 v[62:65], v[222:225], v[166:169], v[62:65]
	s_waitcnt lgkmcnt(1)
	v_mfma_f32_16x16x32_bf16 v[66:69], v[210:213], v[226:229], v[66:69]
	ds_read_b128 v[166:169], v235 offset:8192
	v_add_u32_e32 v230, 0xfffa8000, v209
	s_add_i32 s44, s43, 0x4000
	v_mfma_f32_16x16x32_bf16 v[70:73], v[214:217], v[226:229], v[70:73]
	s_mov_b32 s45, m0
	s_mov_b32 m0, s44
	s_nop 0
	global_load_lds_dwordx4 v230, s[14:15]
	s_mov_b32 m0, s45
	v_mfma_f32_16x16x32_bf16 v[74:77], v[218:221], v[226:229], v[74:77]
	v_mfma_f32_16x16x32_bf16 v[78:81], v[222:225], v[226:229], v[78:81]
	s_waitcnt lgkmcnt(1)
	v_mfma_f32_16x16x32_bf16 v[82:85], v[210:213], v[162:165], v[82:85]
	ds_read_b128 v[226:229], v235 offset:10240
	s_addk_i32 s43, 0x6000
	s_mov_b32 s44, m0
	s_mov_b32 m0, s43
	s_nop 0
	global_load_lds_dwordx4 v209, s[14:15]
	s_mov_b32 m0, s44
	v_mfma_f32_16x16x32_bf16 v[86:89], v[214:217], v[162:165], v[86:89]
	v_mfma_f32_16x16x32_bf16 v[90:93], v[218:221], v[162:165], v[90:93]
	v_mfma_f32_16x16x32_bf16 v[94:97], v[222:225], v[162:165], v[94:97]
	ds_read_b128 v[230:233], v235 offset:12288
	ds_read_b64_tr_b16 v[162:163], v234 offset:16384
	ds_read_b64_tr_b16 v[164:165], v234 offset:18432
	s_waitcnt lgkmcnt(4)
	v_mfma_f32_16x16x32_bf16 v[98:101], v[210:213], v[166:169], v[98:101]
	v_mfma_f32_16x16x32_bf16 v[102:105], v[214:217], v[166:169], v[102:105]
	v_mfma_f32_16x16x32_bf16 v[106:109], v[218:221], v[166:169], v[106:109]
	v_mfma_f32_16x16x32_bf16 v[110:113], v[222:225], v[166:169], v[110:113]
	ds_read_b128 v[234:237], v235 offset:14336
	ds_read_b64_tr_b16 v[166:167], v238 offset:16384
	ds_read_b64_tr_b16 v[168:169], v238 offset:18432
	s_waitcnt lgkmcnt(6)
	v_mfma_f32_16x16x32_bf16 v[114:117], v[210:213], v[226:229], v[114:117]
	v_mfma_f32_16x16x32_bf16 v[118:121], v[214:217], v[226:229], v[118:121]
	v_mfma_f32_16x16x32_bf16 v[122:125], v[218:221], v[226:229], v[122:125]
	v_mfma_f32_16x16x32_bf16 v[126:129], v[222:225], v[226:229], v[126:129]
	v_add_u32_e32 v243, s41, v208
	ds_read_b128 v[226:229], v243
	ds_read_b64_tr_b16 v[238:239], v240 offset:16384
	ds_read_b64_tr_b16 v[240:241], v240 offset:18432
	s_waitcnt lgkmcnt(8)
	v_mfma_f32_16x16x32_bf16 v[130:133], v[210:213], v[230:233], v[130:133]
	v_mfma_f32_16x16x32_bf16 v[134:137], v[214:217], v[230:233], v[134:137]
	v_mfma_f32_16x16x32_bf16 v[138:141], v[218:221], v[230:233], v[138:141]
	v_mfma_f32_16x16x32_bf16 v[142:145], v[222:225], v[230:233], v[142:145]
	s_waitcnt lgkmcnt(5)
	v_mfma_f32_16x16x32_bf16 v[146:149], v[210:213], v[234:237], v[146:149]
	ds_read_b128 v[210:213], v243 offset:2048
	s_add_i32 s41, s24, s42
	v_mfma_f32_16x16x32_bf16 v[150:153], v[214:217], v[234:237], v[150:153]
	ds_read_b64_tr_b16 v[214:215], v242 offset:16384
	ds_read_b64_tr_b16 v[216:217], v242 offset:18432
	v_mfma_f32_16x16x32_bf16 v[158:161], v[218:221], v[234:237], v[158:161]
	v_mfma_f32_16x16x32_bf16 v[154:157], v[222:225], v[234:237], v[154:157]
	ds_read_b128 v[218:221], v243 offset:4096
	s_waitcnt lgkmcnt(6)
	v_mfma_f32_16x16x32_bf16 v[34:37], v[162:165], v[226:229], v[34:37]
	s_add_u32 s44, s2, s16
	s_waitcnt vmcnt(11)
	s_addc_u32 s45, s38, s17
	v_mfma_f32_16x16x32_bf16 v[38:41], v[166:169], v[226:229], v[38:41]
	v_cvt_pk_bf16_f32 v30, v30, v31
	v_cvt_pk_bf16_f32 v31, v32, v33
	v_add_u32_e32 v230, s41, v206
	s_waitcnt lgkmcnt(4)
	v_mfma_f32_16x16x32_bf16 v[42:45], v[238:241], v[226:229], v[42:45]
	s_add_u32 s42, s44, 0x100000
	ds_write_b64 v230, v[30:31]
	s_addc_u32 s43, s45, 0
	s_waitcnt lgkmcnt(2)
	v_mfma_f32_16x16x32_bf16 v[46:49], v[214:217], v[226:229], v[46:49]
	global_load_dwordx4 v[30:33], v199, s[42:43] nt
	v_mfma_f32_16x16x32_bf16 v[50:53], v[162:165], v[210:213], v[50:53]
	ds_read_b128 v[222:225], v243 offset:6144
	s_waitcnt vmcnt(11)
	v_add_u32_e32 v226, s41, v205
	v_mfma_f32_16x16x32_bf16 v[54:57], v[166:169], v[210:213], v[54:57]
	v_cvt_pk_bf16_f32 v26, v26, v27
	v_cvt_pk_bf16_f32 v27, v28, v29
	s_add_u32 s42, s44, 0x110000
	v_mfma_f32_16x16x32_bf16 v[58:61], v[238:241], v[210:213], v[58:61]
	ds_write_b64 v226, v[26:27] offset:4096
	s_addc_u32 s43, s45, 0
	global_load_dwordx4 v[26:29], v199, s[42:43] nt
	v_mfma_f32_16x16x32_bf16 v[62:65], v[214:217], v[210:213], v[62:65]
	s_waitcnt lgkmcnt(3)
	v_mfma_f32_16x16x32_bf16 v[66:69], v[162:165], v[218:221], v[66:69]
	ds_read_b128 v[210:213], v243 offset:8192
	s_waitcnt vmcnt(11)
	s_add_u32 s42, s44, 0x120000
	v_mfma_f32_16x16x32_bf16 v[70:73], v[166:169], v[218:221], v[70:73]
	v_cvt_pk_bf16_f32 v22, v22, v23
	v_cvt_pk_bf16_f32 v23, v24, v25
	ds_write_b64 v230, v[22:23] offset:8192
	v_mfma_f32_16x16x32_bf16 v[74:77], v[238:241], v[218:221], v[74:77]
	s_addc_u32 s43, s45, 0
	global_load_dwordx4 v[22:25], v199, s[42:43] nt
	v_mfma_f32_16x16x32_bf16 v[78:81], v[214:217], v[218:221], v[78:81]
	s_waitcnt lgkmcnt(3)
	v_mfma_f32_16x16x32_bf16 v[82:85], v[162:165], v[222:225], v[82:85]
	ds_read_b128 v[218:221], v243 offset:10240
	s_waitcnt vmcnt(11)
	s_add_u32 s42, s44, 0x130000
	v_mfma_f32_16x16x32_bf16 v[86:89], v[166:169], v[222:225], v[86:89]
	v_cvt_pk_bf16_f32 v18, v18, v19
	v_cvt_pk_bf16_f32 v19, v20, v21
	ds_write_b64 v226, v[18:19] offset:12288
	v_mfma_f32_16x16x32_bf16 v[90:93], v[238:241], v[222:225], v[90:93]
	s_addc_u32 s43, s45, 0
	global_load_dwordx4 v[18:21], v199, s[42:43] nt
	v_mfma_f32_16x16x32_bf16 v[94:97], v[214:217], v[222:225], v[94:97]
	s_waitcnt lgkmcnt(3)
	v_mfma_f32_16x16x32_bf16 v[98:101], v[162:165], v[210:213], v[98:101]
	ds_read_b128 v[222:225], v243 offset:12288
	s_waitcnt vmcnt(11)
	s_add_u32 s42, s44, 0x140000
	v_mfma_f32_16x16x32_bf16 v[102:105], v[166:169], v[210:213], v[102:105]
	v_cvt_pk_bf16_f32 v14, v14, v15
	v_cvt_pk_bf16_f32 v15, v16, v17
	ds_write_b64 v230, v[14:15] offset:16384
	v_mfma_f32_16x16x32_bf16 v[106:109], v[238:241], v[210:213], v[106:109]
	s_addc_u32 s43, s45, 0
	global_load_dwordx4 v[14:17], v199, s[42:43] nt
	v_mfma_f32_16x16x32_bf16 v[110:113], v[214:217], v[210:213], v[110:113]
	s_waitcnt lgkmcnt(3)
	v_mfma_f32_16x16x32_bf16 v[114:117], v[162:165], v[218:221], v[114:117]
	ds_read_b128 v[210:213], v243 offset:14336
	s_waitcnt vmcnt(11)
	s_add_u32 s42, s44, 0x150000
	v_mfma_f32_16x16x32_bf16 v[118:121], v[166:169], v[218:221], v[118:121]
	v_cvt_pk_bf16_f32 v10, v10, v11
	v_cvt_pk_bf16_f32 v11, v12, v13
	ds_write_b64 v226, v[10:11] offset:20480
	v_mfma_f32_16x16x32_bf16 v[122:125], v[238:241], v[218:221], v[122:125]
	s_addc_u32 s43, s45, 0
	global_load_dwordx4 v[10:13], v199, s[42:43] nt
	v_mfma_f32_16x16x32_bf16 v[126:129], v[214:217], v[218:221], v[126:129]
	s_waitcnt lgkmcnt(3)
	v_mfma_f32_16x16x32_bf16 v[130:133], v[162:165], v[222:225], v[130:133]
	s_waitcnt vmcnt(11)
	s_add_u32 s42, s44, 0x160000
	v_cvt_pk_bf16_f32 v6, v6, v7
	v_mfma_f32_16x16x32_bf16 v[134:137], v[166:169], v[222:225], v[134:137]
	v_cvt_pk_bf16_f32 v7, v8, v9
	ds_write_b64 v230, v[6:7] offset:24576
	s_addc_u32 s43, s45, 0
	v_mfma_f32_16x16x32_bf16 v[138:141], v[238:241], v[222:225], v[138:141]
	global_load_dwordx4 v[6:9], v199, s[42:43] nt
	v_mfma_f32_16x16x32_bf16 v[142:145], v[214:217], v[222:225], v[142:145]
	s_waitcnt lgkmcnt(2)
	v_mfma_f32_16x16x32_bf16 v[146:149], v[162:165], v[210:213], v[146:149]
	s_waitcnt vmcnt(11)
	s_add_u32 s42, s44, 0x170000
	v_cvt_pk_bf16_f32 v2, v2, v3
	v_mfma_f32_16x16x32_bf16 v[150:153], v[166:169], v[210:213], v[150:153]
	v_cvt_pk_bf16_f32 v3, v4, v5
	ds_write_b64 v226, v[2:3] offset:28672
	s_addc_u32 s43, s45, 0
	v_mfma_f32_16x16x32_bf16 v[158:161], v[238:241], v[210:213], v[158:161]
	global_load_dwordx4 v[2:5], v199, s[42:43] nt
	v_mfma_f32_16x16x32_bf16 v[154:157], v[214:217], v[210:213], v[154:157]
	s_add_i32 s41, s40, 0x8000
	s_cmp_lg_u32 s40, 0x10000
	s_cselect_b32 s40, s41, 0
	s_add_i32 s41, s39, 0x8000
	s_cmp_lg_u32 s39, 0x10000
	s_waitcnt lgkmcnt(0)
	s_barrier
	s_cselect_b32 s39, s41, 0
	s_add_u32 s16, s16, 0x80000
	s_addc_u32 s17, s17, 0
	s_add_i32 s37, s37, 0x8000
	s_cmp_lg_u32 s16, 0x1500000
	v_add_u32_e32 v209, 0x80, v209
	s_cbranch_scc1 .LBB0_1540
	v_add_u32_e32 v209, s24, v183
	v_add_u32_e32 v242, 0, v207
	v_add_u32_e32 v207, s24, v179
	v_add_u32_e32 v243, s24, v172
	v_add_u32_e32 v236, s24, v181
	ds_read_b64_tr_b16 v[162:163], v209
	ds_read_b64_tr_b16 v[164:165], v209 offset:2048
	ds_read_b64_tr_b16 v[166:167], v236
	ds_read_b64_tr_b16 v[168:169], v236 offset:2048
	ds_read_b128 v[210:213], v242
	ds_read_b128 v[214:217], v242 offset:2048
	ds_read_b64_tr_b16 v[218:219], v207
	ds_read_b64_tr_b16 v[220:221], v207 offset:2048
	ds_read_b64_tr_b16 v[222:223], v243
	ds_read_b64_tr_b16 v[224:225], v243 offset:2048
	s_waitcnt lgkmcnt(5)
	v_mfma_f32_16x16x32_bf16 v[34:37], v[162:165], v[210:213], v[34:37]
	ds_read_b128 v[226:229], v242 offset:4096
	v_mfma_f32_16x16x32_bf16 v[38:41], v[166:169], v[210:213], v[38:41]
	s_waitcnt lgkmcnt(3)
	v_mfma_f32_16x16x32_bf16 v[42:45], v[218:221], v[210:213], v[42:45]
	s_waitcnt lgkmcnt(1)
	v_mfma_f32_16x16x32_bf16 v[46:49], v[222:225], v[210:213], v[46:49]
	v_mfma_f32_16x16x32_bf16 v[50:53], v[162:165], v[214:217], v[50:53]
	ds_read_b128 v[210:213], v242 offset:6144
	v_mfma_f32_16x16x32_bf16 v[54:57], v[166:169], v[214:217], v[54:57]
	v_mfma_f32_16x16x32_bf16 v[58:61], v[218:221], v[214:217], v[58:61]
	v_mfma_f32_16x16x32_bf16 v[62:65], v[222:225], v[214:217], v[62:65]
	s_waitcnt lgkmcnt(1)
	v_mfma_f32_16x16x32_bf16 v[66:69], v[162:165], v[226:229], v[66:69]
	ds_read_b128 v[214:217], v242 offset:8192
	v_mfma_f32_16x16x32_bf16 v[70:73], v[166:169], v[226:229], v[70:73]
	v_mfma_f32_16x16x32_bf16 v[74:77], v[218:221], v[226:229], v[74:77]
	v_mfma_f32_16x16x32_bf16 v[78:81], v[222:225], v[226:229], v[78:81]
	s_waitcnt lgkmcnt(1)
	v_mfma_f32_16x16x32_bf16 v[82:85], v[162:165], v[210:213], v[82:85]
	ds_read_b128 v[226:229], v242 offset:10240
	v_mfma_f32_16x16x32_bf16 v[86:89], v[166:169], v[210:213], v[86:89]
	v_mfma_f32_16x16x32_bf16 v[90:93], v[218:221], v[210:213], v[90:93]
	v_mfma_f32_16x16x32_bf16 v[94:97], v[222:225], v[210:213], v[94:97]
	ds_read_b128 v[210:213], v242 offset:12288
	ds_read_b64_tr_b16 v[230:231], v209 offset:16384
	ds_read_b64_tr_b16 v[232:233], v209 offset:18432
	s_waitcnt lgkmcnt(4)
	v_mfma_f32_16x16x32_bf16 v[98:101], v[162:165], v[214:217], v[98:101]
	v_mfma_f32_16x16x32_bf16 v[102:105], v[166:169], v[214:217], v[102:105]
	v_mfma_f32_16x16x32_bf16 v[106:109], v[218:221], v[214:217], v[106:109]
	v_mfma_f32_16x16x32_bf16 v[110:113], v[222:225], v[214:217], v[110:113]
	ds_read_b128 v[214:217], v242 offset:14336
	ds_read_b64_tr_b16 v[234:235], v236 offset:16384
	ds_read_b64_tr_b16 v[236:237], v236 offset:18432
	s_waitcnt lgkmcnt(6)
	v_mfma_f32_16x16x32_bf16 v[114:117], v[162:165], v[226:229], v[114:117]
	v_mfma_f32_16x16x32_bf16 v[118:121], v[166:169], v[226:229], v[118:121]
	v_mfma_f32_16x16x32_bf16 v[122:125], v[218:221], v[226:229], v[122:125]
	v_mfma_f32_16x16x32_bf16 v[126:129], v[222:225], v[226:229], v[126:129]
	v_add_u32_e32 v244, 0, v208
	ds_read_b128 v[226:229], v244
	ds_read_b64_tr_b16 v[238:239], v207 offset:16384
	ds_read_b64_tr_b16 v[240:241], v207 offset:18432
	s_waitcnt lgkmcnt(8)
	v_mfma_f32_16x16x32_bf16 v[130:133], v[162:165], v[210:213], v[130:133]
	v_mfma_f32_16x16x32_bf16 v[134:137], v[166:169], v[210:213], v[134:137]
	v_mfma_f32_16x16x32_bf16 v[138:141], v[218:221], v[210:213], v[138:141]
	v_mfma_f32_16x16x32_bf16 v[142:145], v[222:225], v[210:213], v[142:145]
	s_waitcnt lgkmcnt(5)
	v_mfma_f32_16x16x32_bf16 v[146:149], v[162:165], v[214:217], v[146:149]
	v_mfma_f32_16x16x32_bf16 v[150:153], v[166:169], v[214:217], v[150:153]
	ds_read_b128 v[162:165], v244 offset:2048
	ds_read_b64_tr_b16 v[166:167], v243 offset:16384
	ds_read_b64_tr_b16 v[168:169], v243 offset:18432
	v_mfma_f32_16x16x32_bf16 v[158:161], v[218:221], v[214:217], v[158:161]
	v_mfma_f32_16x16x32_bf16 v[154:157], v[222:225], v[214:217], v[154:157]
	ds_read_b128 v[208:211], v244 offset:4096
	s_waitcnt vmcnt(7)
	v_add_u32_e32 v206, s25, v206
	v_cvt_pk_bf16_f32 v30, v30, v31
	v_cvt_pk_bf16_f32 v31, v32, v33
	s_waitcnt lgkmcnt(6)
	v_mfma_f32_16x16x32_bf16 v[34:37], v[230:233], v[226:229], v[34:37]
	ds_write_b64 v206, v[30:31]
	v_mfma_f32_16x16x32_bf16 v[38:41], v[234:237], v[226:229], v[38:41]
	s_waitcnt lgkmcnt(5)
	v_mfma_f32_16x16x32_bf16 v[42:45], v[238:241], v[226:229], v[42:45]
	s_waitcnt lgkmcnt(2)
	v_mfma_f32_16x16x32_bf16 v[30:33], v[166:169], v[226:229], v[46:49]
	v_mfma_f32_16x16x32_bf16 v[46:49], v[230:233], v[162:165], v[50:53]
	v_add_u32_e32 v205, s25, v205
	v_mfma_f32_16x16x32_bf16 v[50:53], v[234:237], v[162:165], v[54:57]
	s_nop 2
	ds_read_b128 v[54:57], v244 offset:6144
	s_waitcnt vmcnt(6)
	v_mfma_f32_16x16x32_bf16 v[58:61], v[238:241], v[162:165], v[58:61]
	v_cvt_pk_bf16_f32 v26, v26, v27
	v_cvt_pk_bf16_f32 v27, v28, v29
	ds_write_b64 v205, v[26:27] offset:4096
	v_mfma_f32_16x16x32_bf16 v[26:29], v[166:169], v[162:165], v[62:65]
	s_waitcnt lgkmcnt(3)
	v_mfma_f32_16x16x32_bf16 v[62:65], v[230:233], v[208:211], v[66:69]
	v_mfma_f32_16x16x32_bf16 v[66:69], v[234:237], v[208:211], v[70:73]
	s_nop 2
	ds_read_b128 v[70:73], v244 offset:8192
	s_waitcnt vmcnt(5)
	v_mfma_f32_16x16x32_bf16 v[74:77], v[238:241], v[208:211], v[74:77]
	v_cvt_pk_bf16_f32 v22, v22, v23
	v_cvt_pk_bf16_f32 v23, v24, v25
	ds_write_b64 v206, v[22:23] offset:8192
	v_mfma_f32_16x16x32_bf16 v[22:25], v[166:169], v[208:211], v[78:81]
	s_waitcnt lgkmcnt(3)
	v_mfma_f32_16x16x32_bf16 v[78:81], v[230:233], v[54:57], v[82:85]
	v_mfma_f32_16x16x32_bf16 v[82:85], v[234:237], v[54:57], v[86:89]
	s_nop 2
	ds_read_b128 v[86:89], v244 offset:10240
	s_waitcnt vmcnt(4)
	v_mfma_f32_16x16x32_bf16 v[90:93], v[238:241], v[54:57], v[90:93]
	v_cvt_pk_bf16_f32 v18, v18, v19
	v_cvt_pk_bf16_f32 v19, v20, v21
	ds_write_b64 v205, v[18:19] offset:12288
	v_mfma_f32_16x16x32_bf16 v[18:21], v[166:169], v[54:57], v[94:97]
	s_waitcnt lgkmcnt(3)
	v_mfma_f32_16x16x32_bf16 v[54:57], v[230:233], v[70:73], v[98:101]
	s_nop 2
	ds_read_b128 v[98:101], v244 offset:12288
	s_waitcnt vmcnt(3)
	v_mfma_f32_16x16x32_bf16 v[94:97], v[234:237], v[70:73], v[102:105]
	v_cvt_pk_bf16_f32 v14, v14, v15
	v_cvt_pk_bf16_f32 v15, v16, v17
	ds_write_b64 v206, v[14:15] offset:16384
	v_mfma_f32_16x16x32_bf16 v[102:105], v[238:241], v[70:73], v[106:109]
	v_mfma_f32_16x16x32_bf16 v[14:17], v[166:169], v[70:73], v[110:113]
	s_nop 2
	ds_read_b128 v[110:113], v244 offset:14336
	s_waitcnt vmcnt(2)
	s_waitcnt lgkmcnt(4)
	v_mfma_f32_16x16x32_bf16 v[70:73], v[230:233], v[86:89], v[114:117]
	v_cvt_pk_bf16_f32 v10, v10, v11
	v_cvt_pk_bf16_f32 v11, v12, v13
	ds_write_b64 v205, v[10:11] offset:20480
	v_mfma_f32_16x16x32_bf16 v[106:109], v[234:237], v[86:89], v[118:121]
	v_mfma_f32_16x16x32_bf16 v[114:117], v[238:241], v[86:89], v[122:125]
	v_mfma_f32_16x16x32_bf16 v[10:13], v[166:169], v[86:89], v[126:129]
	s_waitcnt vmcnt(1)
	s_waitcnt lgkmcnt(3)
	v_mfma_f32_16x16x32_bf16 v[86:89], v[230:233], v[98:101], v[130:133]
	v_cvt_pk_bf16_f32 v6, v6, v7
	v_cvt_pk_bf16_f32 v7, v8, v9
	ds_write_b64 v206, v[6:7] offset:24576
	v_mfma_f32_16x16x32_bf16 v[118:121], v[234:237], v[98:101], v[134:137]
	v_mfma_f32_16x16x32_bf16 v[122:125], v[238:241], v[98:101], v[138:141]
	v_mfma_f32_16x16x32_bf16 v[6:9], v[166:169], v[98:101], v[142:145]
	s_waitcnt vmcnt(0)
	s_waitcnt lgkmcnt(2)
	v_mfma_f32_16x16x32_bf16 v[98:101], v[230:233], v[110:113], v[146:149]
	v_cvt_pk_bf16_f32 v2, v2, v3
	v_cvt_pk_bf16_f32 v3, v4, v5
	ds_write_b64 v205, v[2:3] offset:28672
	v_mfma_f32_16x16x32_bf16 v[126:129], v[234:237], v[110:113], v[150:153]
	v_mfma_f32_16x16x32_bf16 v[130:133], v[238:241], v[110:113], v[158:161]
	v_mfma_f32_16x16x32_bf16 v[2:5], v[166:169], v[110:113], v[154:157]
	s_waitcnt lgkmcnt(0)
	s_barrier
	v_add_u32_e32 v168, s25, v183
	v_add_u32_e32 v181, s25, v181
	v_add_u32_e32 v179, s25, v179
	ds_read_b64_tr_b16 v[110:111], v168
	ds_read_b64_tr_b16 v[112:113], v168 offset:2048
	ds_read_b64_tr_b16 v[134:135], v181
	ds_read_b64_tr_b16 v[136:137], v181 offset:2048
	ds_read_b128 v[138:141], v242 offset:32768
	ds_read_b64_tr_b16 v[142:143], v179
	ds_read_b128 v[146:149], v242 offset:34816
	ds_read_b128 v[150:153], v242 offset:36864
	ds_read_b64_tr_b16 v[144:145], v179 offset:2048
	v_add_u32_e32 v172, s25, v172
	ds_read_b64_tr_b16 v[154:155], v172
	ds_read_b64_tr_b16 v[156:157], v172 offset:2048
	s_waitcnt lgkmcnt(6)
	v_mfma_f32_16x16x32_bf16 v[34:37], v[110:113], v[138:141], v[34:37]
	v_mfma_f32_16x16x32_bf16 v[38:41], v[134:137], v[138:141], v[38:41]
	s_waitcnt lgkmcnt(2)
	v_mfma_f32_16x16x32_bf16 v[42:45], v[142:145], v[138:141], v[42:45]
	s_waitcnt lgkmcnt(0)
	v_mfma_f32_16x16x32_bf16 v[30:33], v[154:157], v[138:141], v[30:33]
	v_mfma_f32_16x16x32_bf16 v[46:49], v[110:113], v[146:149], v[46:49]
	ds_read_b128 v[138:141], v242 offset:38912
	v_mfma_f32_16x16x32_bf16 v[50:53], v[134:137], v[146:149], v[50:53]
	v_mfma_f32_16x16x32_bf16 v[58:61], v[142:145], v[146:149], v[58:61]
	v_mfma_f32_16x16x32_bf16 v[26:29], v[154:157], v[146:149], v[26:29]
	v_mfma_f32_16x16x32_bf16 v[62:65], v[110:113], v[150:153], v[62:65]
	ds_read_b128 v[146:149], v242 offset:40960
	v_mfma_f32_16x16x32_bf16 v[66:69], v[134:137], v[150:153], v[66:69]
	v_mfma_f32_16x16x32_bf16 v[74:77], v[142:145], v[150:153], v[74:77]
	v_mfma_f32_16x16x32_bf16 v[22:25], v[154:157], v[150:153], v[22:25]
	s_waitcnt lgkmcnt(1)
	v_mfma_f32_16x16x32_bf16 v[150:153], v[134:137], v[138:141], v[82:85]
	s_nop 2
	ds_read_b128 v[82:85], v242 offset:43008
	v_mfma_f32_16x16x32_bf16 v[78:81], v[110:113], v[138:141], v[78:81]
	v_mfma_f32_16x16x32_bf16 v[18:21], v[154:157], v[138:141], v[18:21]
	v_mfma_f32_16x16x32_bf16 v[158:161], v[142:145], v[138:141], v[90:93]
	s_nop 2
	ds_read_b128 v[90:93], v242 offset:45056
	ds_read_b64_tr_b16 v[166:167], v168 offset:16384
	ds_read_b64_tr_b16 v[168:169], v168 offset:18432
	s_waitcnt lgkmcnt(4)
	v_mfma_f32_16x16x32_bf16 v[54:57], v[110:113], v[146:149], v[54:57]
	v_mfma_f32_16x16x32_bf16 v[14:17], v[154:157], v[146:149], v[14:17]
	v_mfma_f32_16x16x32_bf16 v[138:141], v[134:137], v[146:149], v[94:97]
	v_mfma_f32_16x16x32_bf16 v[162:165], v[142:145], v[146:149], v[102:105]
	s_waitcnt lgkmcnt(3)
	v_mfma_f32_16x16x32_bf16 v[146:149], v[110:113], v[82:85], v[70:73]
	s_nop 2
	ds_read_b128 v[70:73], v242 offset:47104
	ds_read_b64_tr_b16 v[214:215], v181 offset:16384
	ds_read_b64_tr_b16 v[216:217], v181 offset:18432
	v_mfma_f32_16x16x32_bf16 v[10:13], v[154:157], v[82:85], v[10:13]
	v_mfma_f32_16x16x32_bf16 v[206:209], v[134:137], v[82:85], v[106:109]
	v_mfma_f32_16x16x32_bf16 v[210:213], v[142:145], v[82:85], v[114:117]
	ds_read_b128 v[82:85], v244 offset:32768
	ds_read_b64_tr_b16 v[230:231], v179 offset:16384
	ds_read_b64_tr_b16 v[232:233], v179 offset:18432
	s_waitcnt lgkmcnt(8)
	v_mfma_f32_16x16x32_bf16 v[6:9], v[154:157], v[90:93], v[6:9]
	v_mfma_f32_16x16x32_bf16 v[218:221], v[110:113], v[90:93], v[86:89]
	v_mfma_f32_16x16x32_bf16 v[222:225], v[134:137], v[90:93], v[118:121]
	v_mfma_f32_16x16x32_bf16 v[226:229], v[142:145], v[90:93], v[122:125]
	s_waitcnt lgkmcnt(5)
	v_mfma_f32_16x16x32_bf16 v[130:133], v[142:145], v[70:73], v[130:133]
	ds_read_b128 v[86:89], v244 offset:34816
	ds_read_b64_tr_b16 v[142:143], v172 offset:16384
	ds_read_b64_tr_b16 v[144:145], v172 offset:18432
	v_mfma_f32_16x16x32_bf16 v[134:137], v[134:137], v[70:73], v[126:129]
	v_mfma_f32_16x16x32_bf16 v[2:5], v[154:157], v[70:73], v[2:5]
	v_mfma_f32_16x16x32_bf16 v[234:237], v[110:113], v[70:73], v[98:101]
	s_waitcnt lgkmcnt(5)
	v_mfma_f32_16x16x32_bf16 v[126:129], v[166:169], v[82:85], v[34:37]
	s_nop 2
	ds_read_b128 v[34:37], v244 offset:36864
	v_mfma_f32_16x16x32_bf16 v[122:125], v[214:217], v[82:85], v[38:41]
	s_waitcnt lgkmcnt(4)
	v_mfma_f32_16x16x32_bf16 v[118:121], v[230:233], v[82:85], v[42:45]
	s_waitcnt lgkmcnt(1)
	v_mfma_f32_16x16x32_bf16 v[114:117], v[142:145], v[82:85], v[30:33]
	s_nop 2
	ds_read_b128 v[30:33], v244 offset:38912
	v_mfma_f32_16x16x32_bf16 v[110:113], v[166:169], v[86:89], v[46:49]
	v_mfma_f32_16x16x32_bf16 v[106:109], v[214:217], v[86:89], v[50:53]
	v_mfma_f32_16x16x32_bf16 v[102:105], v[230:233], v[86:89], v[58:61]
	v_mfma_f32_16x16x32_bf16 v[98:101], v[142:145], v[86:89], v[26:29]
	s_nop 2
	ds_read_b128 v[26:29], v244 offset:40960
	s_waitcnt lgkmcnt(2)
	v_mfma_f32_16x16x32_bf16 v[94:97], v[166:169], v[34:37], v[62:65]
	v_mfma_f32_16x16x32_bf16 v[90:93], v[214:217], v[34:37], v[66:69]
	v_mfma_f32_16x16x32_bf16 v[86:89], v[230:233], v[34:37], v[74:77]
	v_mfma_f32_16x16x32_bf16 v[82:85], v[142:145], v[34:37], v[22:25]
	s_nop 2
	ds_read_b128 v[22:25], v244 offset:43008
	s_waitcnt lgkmcnt(2)
	v_mfma_f32_16x16x32_bf16 v[78:81], v[166:169], v[30:33], v[78:81]
	v_mfma_f32_16x16x32_bf16 v[74:77], v[214:217], v[30:33], v[150:153]
	v_mfma_f32_16x16x32_bf16 v[70:73], v[230:233], v[30:33], v[158:161]
	v_mfma_f32_16x16x32_bf16 v[66:69], v[142:145], v[30:33], v[18:21]
	s_nop 2
	ds_read_b128 v[18:21], v244 offset:45056
	s_waitcnt lgkmcnt(2)
	v_mfma_f32_16x16x32_bf16 v[62:65], v[166:169], v[26:29], v[54:57]
	v_mfma_f32_16x16x32_bf16 v[58:61], v[214:217], v[26:29], v[138:141]
	v_mfma_f32_16x16x32_bf16 v[54:57], v[230:233], v[26:29], v[162:165]
	v_mfma_f32_16x16x32_bf16 v[50:53], v[142:145], v[26:29], v[14:17]
	s_waitcnt lgkmcnt(1)
	v_mfma_f32_16x16x32_bf16 v[46:49], v[166:169], v[22:25], v[146:149]
	ds_read_b128 v[138:141], v244 offset:47104
	v_mfma_f32_16x16x32_bf16 v[42:45], v[214:217], v[22:25], v[206:209]
	v_mfma_f32_16x16x32_bf16 v[38:41], v[230:233], v[22:25], v[210:213]
	v_mfma_f32_16x16x32_bf16 v[34:37], v[142:145], v[22:25], v[10:13]
	s_waitcnt lgkmcnt(1)
	v_mfma_f32_16x16x32_bf16 v[30:33], v[166:169], v[18:21], v[218:221]
	v_mfma_f32_16x16x32_bf16 v[26:29], v[214:217], v[18:21], v[222:225]
	v_mfma_f32_16x16x32_bf16 v[22:25], v[230:233], v[18:21], v[226:229]
	v_mfma_f32_16x16x32_bf16 v[18:21], v[142:145], v[18:21], v[6:9]
	s_waitcnt lgkmcnt(0)
	v_mfma_f32_16x16x32_bf16 v[14:17], v[166:169], v[138:141], v[234:237]
	v_mfma_f32_16x16x32_bf16 v[10:13], v[214:217], v[138:141], v[134:137]
	v_mfma_f32_16x16x32_bf16 v[6:9], v[230:233], v[138:141], v[130:133]
	v_mfma_f32_16x16x32_bf16 v[2:5], v[142:145], v[138:141], v[2:5]
	s_waitcnt lgkmcnt(0)
	s_barrier
	s_nop 0
	v_mov_b32_e32 v131, 0
	s_andn2_b64 vcc, exec, s[12:13]
	v_mov_b32_e32 v133, 0
	v_mov_b32_e32 v134, 0
	s_cbranch_vccnz .LBB0_1536
	global_load_dword v131, v[184:185], off
	global_load_dword v133, v[186:187], off
	global_load_dword v134, v[188:189], off
	s_branch .LBB0_1536
